# speedup vs baseline: 1.0118x; 1.0118x over previous
.LBB3_33:
	s_or_b64 exec, exec, s[4:5]
	s_add_u32 s4, s20, 0x100000
	s_mul_hi_u32 s2, s26, 0xaaaaaaab
	s_addc_u32 s5, s21, 0
	s_lshr_b32 s6, s2, 8
	s_mul_hi_u32 s2, s27, 0x2aaaaaab
	s_mul_i32 s2, s2, 6
	s_sub_i32 s2, s27, s2
	s_waitcnt vmcnt(5)
	v_mov_b32_e32 v2, s2
	v_sub_co_u32_e64 v3, s[2:3], s2, 3
	v_mov_b32_e32 v85, 0
	s_nop 0
	v_cndmask_b32_e64 v2, v3, v2, s[2:3]
	s_and_b64 s[2:3], s[2:3], exec
	s_cselect_b32 s2, s28, s29
	s_mul_i32 s2, s2, 49
	s_add_i32 s2, s2, s6
	s_mul_hi_u32 s3, s2, 3
	s_mul_i32 s2, s2, 3
	v_mov_b32_e32 v3, v85
	v_lshl_add_u64 v[2:3], s[2:3], 0, v[2:3]
	s_add_i32 s2, s27, 4
	s_mul_hi_u32 s6, s2, 0x2aaaaaab
	v_lshlrev_b64 v[2:3], 10, v[2:3]
	s_mul_i32 s3, s6, 6
	v_lshlrev_b32_e32 v84, 4, v92
	v_lshl_add_u64 v[2:3], s[4:5], 0, v[2:3]
	s_sub_i32 s2, s2, s3
	v_lshl_add_u64 v[86:87], v[2:3], 0, v[84:85]
	v_mov_b32_e32 v2, s2
	v_sub_co_u32_e64 v3, s[2:3], s2, 3
	s_nop 1
	v_cndmask_b32_e64 v2, v3, v2, s[2:3]
	s_and_b64 s[2:3], s[2:3], exec
	s_cselect_b32 s2, s28, s29
	s_mul_i32 s2, s2, 49
	s_add_i32 s2, s2, s6
	s_mul_hi_u32 s3, s2, 3
	s_mul_i32 s2, s2, 3
	v_mov_b32_e32 v3, v85
	v_lshl_add_u64 v[2:3], s[2:3], 0, v[2:3]
	s_add_i32 s2, s27, 8
	s_mul_hi_u32 s6, s2, 0x2aaaaaab
	v_lshlrev_b64 v[2:3], 10, v[2:3]
	s_mul_i32 s3, s6, 6
	v_lshl_add_u64 v[2:3], s[4:5], 0, v[2:3]
	s_sub_i32 s2, s2, s3
	v_lshl_add_u64 v[88:89], v[2:3], 0, v[84:85]
	v_mov_b32_e32 v2, s2
	v_sub_co_u32_e64 v3, s[2:3], s2, 3
	s_nop 1
	v_cndmask_b32_e64 v2, v3, v2, s[2:3]
	s_and_b64 s[2:3], s[2:3], exec
	s_cselect_b32 s2, s28, s29
	s_mul_i32 s2, s2, 49
	s_add_i32 s2, s2, s6
	s_mul_hi_u32 s3, s2, 3
	s_mul_i32 s2, s2, 3
	v_mov_b32_e32 v3, v85
	v_lshl_add_u64 v[2:3], s[2:3], 0, v[2:3]
	v_lshlrev_b64 v[2:3], 10, v[2:3]
	v_lshl_add_u64 v[2:3], s[4:5], 0, v[2:3]
	s_and_b32 s2, s26, 0xfffffc0
	v_lshl_add_u64 v[90:91], v[2:3], 0, v[84:85]
	v_lshl_or_b32 v93, s2, 4, v84
	v_readfirstlane_b32 s40, v86
	v_readfirstlane_b32 s41, v87
	v_readfirstlane_b32 s42, v88
	v_readfirstlane_b32 s43, v89
	v_readfirstlane_b32 s44, v90
	v_readfirstlane_b32 s45, v91
	s_lshl_b32 s46, s27, 10
	s_add_u32 s47, s46, 0x1000
	s_add_u32 s48, s46, 0x2000
	s_movk_i32 s50, 0xc00
	s_movk_i32 s51, 0x1800
	s_cmp_ge_u32 s27, 2
	s_cselect_b32 s49, s50, s51
	v_and_b32_e32 v99, 31, v92
	v_mov_b32_e32 v79, 0x150
	v_cmp_gt_u32_e64 s[52:53], 21, v99
	s_cmp_eq_u32 s27, 2
	s_cselect_b64 s[54:55], -1, 0
	v_cndmask_b32_e64 v99, v79, v84, s[52:53]
	s_cmp_eq_u32 s27, 1
	s_cselect_b64 s[56:57], -1, 0
	s_or_b64 s[58:59], s[54:55], s[56:57]
	s_not_b64 s[58:59], s[58:59]
	v_cndmask_b32_e64 v76, v84, v99, s[54:55]
	v_cndmask_b32_e64 v77, v84, v99, s[56:57]
	v_cndmask_b32_e64 v78, v84, v99, s[58:59]
	s_waitcnt lgkmcnt(0)
	s_nop 4
	s_andn2_b64 vcc, exec, vcc
	s_mov_b64 s[2:3], -1
	s_cbranch_vccnz .LBB3_35
	s_add_u32 m0, s46, 0x0
	s_nop 0
	global_load_lds_dwordx4 v76, s[40:41]
	s_add_u32 m0, s47, 0x0
	s_nop 0
	global_load_lds_dwordx4 v77, s[42:43]
	s_add_u32 m0, s48, 0x0
	s_nop 0
	global_load_lds_dwordx4 v78, s[44:45]
	s_add_u32 m0, s46, 0x3000
	s_add_u32 s40, s40, 0x1800
	s_addc_u32 s41, s41, 0
	global_load_lds_dwordx4 v76, s[40:41]
	s_add_u32 m0, s47, 0x3000
	s_add_u32 s42, s42, 0x1800
	s_addc_u32 s43, s43, 0
	global_load_lds_dwordx4 v77, s[42:43]
	s_add_u32 m0, s48, 0x3000
	s_add_u32 s44, s44, 0x1800
	s_addc_u32 s45, s45, 0
	global_load_lds_dwordx4 v78, s[44:45]
	s_add_u32 m0, s46, 0xd3c0
	s_add_u32 s40, s40, 0x1800
	s_addc_u32 s41, s41, 0
	global_load_lds_dwordx4 v76, s[40:41]
	s_add_u32 m0, s47, 0xd3c0
	s_add_u32 s42, s42, 0x1800
	s_addc_u32 s43, s43, 0
	global_load_lds_dwordx4 v77, s[42:43]
	s_add_u32 m0, s48, 0xd3c0
	s_add_u32 s44, s44, 0x1800
	s_addc_u32 s45, s45, 0
	global_load_lds_dwordx4 v78, s[44:45]
	s_add_u32 m0, s46, 0x103c0
	s_add_u32 s40, s40, 0x1800
	s_addc_u32 s41, s41, 0
	global_load_lds_dwordx4 v76, s[40:41]
	s_add_u32 m0, s47, 0x103c0
	s_add_u32 s42, s42, 0x1800
	s_addc_u32 s43, s43, 0
	global_load_lds_dwordx4 v77, s[42:43]
	s_add_u32 m0, s48, 0x103c0
	s_add_u32 s44, s44, 0x1800
	s_addc_u32 s45, s45, 0
	global_load_lds_dwordx4 v78, s[44:45]
	s_waitcnt vmcnt(9)
	s_barrier
	s_waitcnt vmcnt(6)
	s_barrier
	s_add_u32 m0, s46, 0x0
	s_add_u32 s40, s40, 0x1800
	s_addc_u32 s41, s41, 0
	global_load_lds_dwordx4 v76, s[40:41]
	s_add_u32 m0, s47, 0x0
	s_add_u32 s42, s42, 0x1800
	s_addc_u32 s43, s43, 0
	global_load_lds_dwordx4 v77, s[42:43]
	s_add_u32 m0, s48, 0x0
	s_add_u32 s44, s44, 0x1800
	s_addc_u32 s45, s45, 0
	global_load_lds_dwordx4 v78, s[44:45]
	s_waitcnt vmcnt(6)
	s_barrier
	s_add_u32 m0, s46, 0x3000
	s_add_u32 s40, s40, 0x1800
	s_addc_u32 s41, s41, 0
	global_load_lds_dwordx4 v76, s[40:41]
	s_add_u32 m0, s47, 0x3000
	s_add_u32 s42, s42, 0x1800
	s_addc_u32 s43, s43, 0
	global_load_lds_dwordx4 v77, s[42:43]
	s_add_u32 m0, s48, 0x3000
	s_add_u32 s44, s44, 0x1800
	s_addc_u32 s45, s45, 0
	global_load_lds_dwordx4 v78, s[44:45]
	s_waitcnt vmcnt(6)
	s_barrier
	s_add_u32 m0, s46, 0xd3c0
	s_add_u32 s40, s40, 0x1800
	s_addc_u32 s41, s41, 0
	global_load_lds_dwordx4 v76, s[40:41]
	s_add_u32 m0, s47, 0xd3c0
	s_add_u32 s42, s42, 0x1800
	s_addc_u32 s43, s43, 0
	global_load_lds_dwordx4 v77, s[42:43]
	s_add_u32 m0, s48, 0xd3c0
	s_add_u32 s44, s44, 0x1800
	s_addc_u32 s45, s45, 0
	global_load_lds_dwordx4 v78, s[44:45]
	s_waitcnt vmcnt(6)
	s_barrier
	s_add_u32 m0, s46, 0x103c0
	s_add_u32 s40, s40, 0x1800
	s_addc_u32 s41, s41, 0
	global_load_lds_dwordx4 v76, s[40:41]
	s_add_u32 m0, s47, 0x103c0
	s_add_u32 s42, s42, 0x1800
	s_addc_u32 s43, s43, 0
	global_load_lds_dwordx4 v77, s[42:43]
	s_add_u32 m0, s48, 0x103c0
	s_add_u32 s44, s44, 0x1800
	s_addc_u32 s45, s45, 0
	global_load_lds_dwordx4 v78, s[44:45]
	s_waitcnt vmcnt(6)
	s_barrier
	s_add_u32 m0, s46, 0x0
	s_add_u32 s40, s40, 0x1800
	s_addc_u32 s41, s41, 0
	global_load_lds_dwordx4 v76, s[40:41]
	s_add_u32 m0, s47, 0x0
	s_add_u32 s42, s42, 0x1800
	s_addc_u32 s43, s43, 0
	global_load_lds_dwordx4 v77, s[42:43]
	s_add_u32 m0, s48, 0x0
	s_add_u32 s44, s44, 0x1800
	s_addc_u32 s45, s45, 0
	global_load_lds_dwordx4 v78, s[44:45]
	s_waitcnt vmcnt(6)
	s_barrier
	s_add_u32 m0, s46, 0x3000
	s_add_u32 s40, s40, 0x1800
	s_addc_u32 s41, s41, 0
	global_load_lds_dwordx4 v76, s[40:41]
	s_add_u32 m0, s47, 0x3000
	s_add_u32 s42, s42, 0x1800
	s_addc_u32 s43, s43, 0
	global_load_lds_dwordx4 v77, s[42:43]
	s_add_u32 m0, s48, 0x3000
	s_add_u32 s44, s44, 0x1800
	s_addc_u32 s45, s45, 0
	global_load_lds_dwordx4 v78, s[44:45]
	s_waitcnt vmcnt(6)
	s_barrier
	s_add_u32 m0, s46, 0xd3c0
	s_add_u32 s40, s40, 0x1800
	s_addc_u32 s41, s41, 0
	global_load_lds_dwordx4 v76, s[40:41]
	s_add_u32 m0, s47, 0xd3c0
	s_add_u32 s42, s42, 0x1800
	s_addc_u32 s43, s43, 0
	global_load_lds_dwordx4 v77, s[42:43]
	s_add_u32 m0, s48, 0xd3c0
	s_add_u32 s44, s44, 0x1800
	s_addc_u32 s45, s45, 0
	global_load_lds_dwordx4 v78, s[44:45]
	s_waitcnt vmcnt(6)
	s_barrier
	s_add_u32 m0, s46, 0x103c0
	s_add_u32 s40, s40, 0x1800
	s_addc_u32 s41, s41, 0
	global_load_lds_dwordx4 v76, s[40:41]
	s_add_u32 m0, s47, 0x103c0
	s_add_u32 s42, s42, 0x1800
	s_addc_u32 s43, s43, 0
	global_load_lds_dwordx4 v77, s[42:43]
	s_add_u32 m0, s48, 0x103c0
	s_add_u32 s44, s44, 0x1800
	s_addc_u32 s45, s45, 0
	global_load_lds_dwordx4 v78, s[44:45]
	s_waitcnt vmcnt(6)
	s_barrier
	s_add_u32 m0, s46, 0x0
	s_add_u32 s40, s40, 0x1800
	s_addc_u32 s41, s41, 0
	global_load_lds_dwordx4 v76, s[40:41]
	s_add_u32 m0, s47, 0x0
	s_add_u32 s42, s42, 0x1800
	s_addc_u32 s43, s43, 0
	global_load_lds_dwordx4 v77, s[42:43]
	s_add_u32 m0, s48, 0x0
	s_add_u32 s44, s44, 0x1800
	s_addc_u32 s45, s45, 0
	global_load_lds_dwordx4 v78, s[44:45]
	s_waitcnt vmcnt(6)
	s_barrier
	s_add_u32 m0, s46, 0x3000
	s_add_u32 s40, s40, 0x1800
	s_addc_u32 s41, s41, 0
	global_load_lds_dwordx4 v76, s[40:41]
	s_add_u32 m0, s47, 0x3000
	s_add_u32 s42, s42, 0x1800
	s_addc_u32 s43, s43, 0
	global_load_lds_dwordx4 v77, s[42:43]
	s_add_u32 m0, s48, 0x3000
	s_add_u32 s44, s44, 0x1800
	s_addc_u32 s45, s45, 0
	global_load_lds_dwordx4 v78, s[44:45]
	s_waitcnt vmcnt(6)
	s_barrier
	s_add_u32 m0, s46, 0xd3c0
	s_add_u32 s40, s40, 0x1800
	s_addc_u32 s41, s41, 0
	global_load_lds_dwordx4 v76, s[40:41]
	s_add_u32 m0, s47, 0xd3c0
	s_add_u32 s42, s42, 0x1800
	s_addc_u32 s43, s43, 0
	global_load_lds_dwordx4 v77, s[42:43]
	s_add_u32 m0, s48, 0xd3c0
	s_add_u32 s44, s44, 0x1800
	s_addc_u32 s45, s45, 0
	global_load_lds_dwordx4 v78, s[44:45]
	s_waitcnt vmcnt(6)
	s_barrier
	s_add_u32 m0, s46, 0x103c0
	s_add_u32 s40, s40, 0x1800
	s_addc_u32 s41, s41, 0
	global_load_lds_dwordx4 v76, s[40:41]
	s_add_u32 m0, s47, 0x103c0
	s_add_u32 s42, s42, 0x1800
	s_addc_u32 s43, s43, 0
	global_load_lds_dwordx4 v77, s[42:43]
	s_add_u32 m0, s48, 0x103c0
	s_add_u32 s44, s44, 0x1800
	s_addc_u32 s45, s45, 0
	global_load_lds_dwordx4 v78, s[44:45]
	s_waitcnt vmcnt(6)
	s_barrier
	s_add_u32 m0, s46, 0x0
	s_add_u32 s40, s40, 0x1800
	s_addc_u32 s41, s41, 0
	global_load_lds_dwordx4 v76, s[40:41]
	s_add_u32 m0, s47, 0x0
	s_add_u32 s42, s42, 0x1800
	s_addc_u32 s43, s43, 0
	global_load_lds_dwordx4 v77, s[42:43]
	s_add_u32 m0, s48, 0x0
	s_add_u32 s44, s44, 0x1800
	s_addc_u32 s45, s45, 0
	global_load_lds_dwordx4 v78, s[44:45]
	s_waitcnt vmcnt(6)
	s_barrier
	s_add_u32 m0, s46, 0x3000
	s_add_u32 s40, s40, 0x1800
	s_addc_u32 s41, s41, 0
	global_load_lds_dwordx4 v76, s[40:41]
	s_add_u32 m0, s47, 0x3000
	s_add_u32 s42, s42, 0x1800
	s_addc_u32 s43, s43, 0
	global_load_lds_dwordx4 v77, s[42:43]
	s_add_u32 m0, s48, 0x3000
	s_add_u32 s44, s44, 0x1800
	s_addc_u32 s45, s45, 0
	global_load_lds_dwordx4 v78, s[44:45]
	s_waitcnt vmcnt(6)
	s_barrier
	s_add_u32 m0, s46, 0xd3c0
	s_add_u32 s40, s40, 0x1800
	s_addc_u32 s41, s41, 0
	global_load_lds_dwordx4 v76, s[40:41]
	s_add_u32 m0, s47, 0xd3c0
	s_add_u32 s42, s42, 0x1800
	s_addc_u32 s43, s43, 0
	global_load_lds_dwordx4 v77, s[42:43]
	s_add_u32 m0, s48, 0xd3c0
	s_add_u32 s44, s44, 0x1800
	s_addc_u32 s45, s45, 0
	global_load_lds_dwordx4 v78, s[44:45]
	s_waitcnt vmcnt(6)
	s_barrier
	s_add_u32 m0, s46, 0x103c0
	s_add_u32 s40, s40, 0x1800
	s_addc_u32 s41, s41, 0
	global_load_lds_dwordx4 v76, s[40:41]
	s_add_u32 m0, s47, 0x103c0
	s_add_u32 s42, s42, 0x1800
	s_addc_u32 s43, s43, 0
	global_load_lds_dwordx4 v77, s[42:43]
	s_add_u32 m0, s48, 0x103c0
	s_add_u32 s44, s44, 0x1800
	s_addc_u32 s45, s45, 0
	global_load_lds_dwordx4 v78, s[44:45]
	s_waitcnt vmcnt(6)
	s_barrier
	s_add_u32 m0, s46, 0x0
	s_add_u32 s40, s40, 0x1800
	s_addc_u32 s41, s41, 0
	global_load_lds_dwordx4 v76, s[40:41]
	s_add_u32 m0, s47, 0x0
	s_add_u32 s42, s42, 0x1800
	s_addc_u32 s43, s43, 0
	global_load_lds_dwordx4 v77, s[42:43]
	s_add_u32 m0, s48, 0x0
	s_add_u32 s44, s44, 0x1800
	s_addc_u32 s45, s45, 0
	global_load_lds_dwordx4 v78, s[44:45]
	s_waitcnt vmcnt(6)
	s_barrier
	s_add_u32 m0, s46, 0x3000
	s_add_u32 s40, s40, 0x1800
	s_addc_u32 s41, s41, 0
	global_load_lds_dwordx4 v76, s[40:41]
	s_add_u32 m0, s47, 0x3000
	s_add_u32 s42, s42, 0x1800
	s_addc_u32 s43, s43, 0
	global_load_lds_dwordx4 v77, s[42:43]
	s_add_u32 m0, s48, 0x3000
	s_add_u32 s44, s44, 0x1800
	s_addc_u32 s45, s45, 0
	global_load_lds_dwordx4 v78, s[44:45]
	s_waitcnt vmcnt(6)
	s_barrier
	s_add_u32 m0, s46, 0xd3c0
	s_add_u32 s40, s40, 0x1800
	s_addc_u32 s41, s41, 0
	global_load_lds_dwordx4 v76, s[40:41]
	s_add_u32 m0, s47, 0xd3c0
	s_add_u32 s42, s42, 0x1800
	s_addc_u32 s43, s43, 0
	global_load_lds_dwordx4 v77, s[42:43]
	s_add_u32 m0, s48, 0xd3c0
	s_add_u32 s44, s44, 0x1800
	s_addc_u32 s45, s45, 0
	global_load_lds_dwordx4 v78, s[44:45]
	s_waitcnt vmcnt(6)
	s_barrier
	s_add_u32 m0, s46, 0x103c0
	s_add_u32 s40, s40, 0x1800
	s_addc_u32 s41, s41, 0
	global_load_lds_dwordx4 v76, s[40:41]
	s_add_u32 m0, s47, 0x103c0
	s_add_u32 s42, s42, 0x1800
	s_addc_u32 s43, s43, 0
	global_load_lds_dwordx4 v77, s[42:43]
	s_add_u32 m0, s48, 0x103c0
	s_add_u32 s44, s44, 0x1800
	s_addc_u32 s45, s45, 0
	global_load_lds_dwordx4 v78, s[44:45]
	s_waitcnt vmcnt(6)
	s_barrier
	s_add_u32 m0, s46, 0x0
	s_add_u32 s40, s40, 0x1800
	s_addc_u32 s41, s41, 0
	global_load_lds_dwordx4 v76, s[40:41]
	s_add_u32 m0, s47, 0x0
	s_add_u32 s42, s42, s49
	s_addc_u32 s43, s43, 0
	global_load_lds_dwordx4 v77, s[42:43]
	s_add_u32 m0, s48, 0x0
	s_add_u32 s44, s44, 0xc00
	s_addc_u32 s45, s45, 0
	global_load_lds_dwordx4 v78, s[44:45]
	s_waitcnt vmcnt(6)
	s_barrier
	s_waitcnt vmcnt(3)
	s_barrier
	s_waitcnt vmcnt(0)
	s_barrier
	s_branch .LBB3_39
.LBB3_35:
	s_andn2_b64 vcc, exec, s[2:3]
	s_cbranch_vccnz .LBB3_39
	s_waitcnt vmcnt(4)
	v_ashrrev_i32_e32 v81, 31, v80
	v_lshl_add_u64 v[2:3], v[80:81], 3, s[20:21]
	v_add_co_u32_e32 v2, vcc, 0x48000, v2
	s_movk_i32 s8, 0x620
	s_nop 0
	v_addc_co_u32_e32 v3, vcc, 0, v3, vcc
	global_load_dwordx2 v[82:83], v[2:3], off
	v_and_b32_e32 v2, 0x70, v7
	v_bitop3_b32 v2, v0, v2, 48 bitop3:0x6c
	s_waitcnt vmcnt(4)
	v_mad_u64_u32 v[64:65], s[6:7], v9, s8, v[2:3]
	v_lshrrev_b32_e32 v3, 4, v92
	v_bitop3_b32 v3, v3, v0, 4 bitop3:0x36
	v_lshlrev_b32_e32 v3, 4, v3
	v_and_b32_e32 v4, 0x70, v3
	s_waitcnt vmcnt(3)
	v_mad_u64_u32 v[66:67], s[6:7], v8, s8, v[4:5]
	s_waitcnt vmcnt(2)
	v_mad_u64_u32 v[68:69], s[6:7], v6, s8, v[2:3]
	s_waitcnt vmcnt(1)
	v_mad_u64_u32 v[70:71], s[6:7], v1, s8, v[4:5]
	v_lshrrev_b32_e32 v85, 5, v92
	v_bfe_u32 v2, v0, 1, 3
	s_mov_b64 s[6:7], 0x1800
	s_add_u32 s4, s20, 0x4000000
	v_bitop3_b32 v32, v85, v2, 2 bitop3:0x36
	v_bitop3_b32 v33, v85, v2, 4 bitop3:0x36
	v_bitop3_b32 v34, v85, v2, 6 bitop3:0x36
	v_lshl_add_u64 v[2:3], v[86:87], 0, s[6:7]
	s_addc_u32 s5, s21, 0
	s_lshl_b32 s2, s27, 12
	s_addk_i32 s2, 0x6000
	v_lshrrev_b32_e32 v1, 1, v0
	v_or_b32_e32 v81, s2, v84
	v_lshlrev_b32_e32 v0, 7, v0
	v_and_b32_e32 v8, 0xf80, v0
	v_lshlrev_b32_e32 v9, 4, v32
	v_bitop3_b32 v1, v85, v1, 7 bitop3:0x78
	v_or3_b32 v96, s2, v9, v8
	v_lshlrev_b32_e32 v9, 4, v33
	v_lshlrev_b32_e32 v1, 4, v1
	v_or3_b32 v97, s2, v9, v8
	v_lshlrev_b32_e32 v9, 4, v34
	v_or3_b32 v95, s2, v1, v8
	v_or3_b32 v94, s2, v9, v8
	v_add_u32_e32 v98, 0x103c0, v84
	global_load_dwordx4 v[116:119], v64, s[4:5] offset:0
	global_load_dwordx4 v[120:123], v66, s[4:5] offset:0
	global_load_dwordx4 v[124:127], v68, s[4:5] offset:0
	global_load_dwordx4 v[128:131], v70, s[4:5] offset:0
	global_load_dwordx4 v[132:135], v64, s[4:5] offset:128
	global_load_dwordx4 v[136:139], v66, s[4:5] offset:128
	global_load_dwordx4 v[140:143], v68, s[4:5] offset:128
	global_load_dwordx4 v[144:147], v70, s[4:5] offset:128
	global_load_dwordx4 v[148:151], v64, s[4:5] offset:256
	global_load_dwordx4 v[152:155], v66, s[4:5] offset:256
	global_load_dwordx4 v[156:159], v68, s[4:5] offset:256
	global_load_dwordx4 v[72:75], v70, s[4:5] offset:256
	s_add_u32 m0, s46, 0x0
	s_nop 0
	global_load_lds_dwordx4 v76, s[40:41]
	s_add_u32 m0, s47, 0x0
	s_nop 0
	global_load_lds_dwordx4 v77, s[42:43]
	s_add_u32 m0, s48, 0x0
	s_nop 0
	global_load_lds_dwordx4 v78, s[44:45]
	s_add_u32 m0, s46, 0x3000
	s_add_u32 s40, s40, 0x1800
	s_addc_u32 s41, s41, 0
	global_load_lds_dwordx4 v76, s[40:41]
	s_add_u32 m0, s47, 0x3000
	s_add_u32 s42, s42, 0x1800
	s_addc_u32 s43, s43, 0
	global_load_lds_dwordx4 v77, s[42:43]
	s_add_u32 m0, s48, 0x3000
	s_add_u32 s44, s44, 0x1800
	s_addc_u32 s45, s45, 0
	global_load_lds_dwordx4 v78, s[44:45]
	s_add_u32 m0, s46, 0xd3c0
	s_add_u32 s40, s40, 0x1800
	s_addc_u32 s41, s41, 0
	global_load_lds_dwordx4 v76, s[40:41]
	s_add_u32 m0, s47, 0xd3c0
	s_add_u32 s42, s42, 0x1800
	s_addc_u32 s43, s43, 0
	global_load_lds_dwordx4 v77, s[42:43]
	s_add_u32 m0, s48, 0xd3c0
	s_add_u32 s44, s44, 0x1800
	s_addc_u32 s45, s45, 0
	global_load_lds_dwordx4 v78, s[44:45]
	s_add_u32 m0, s46, 0x103c0
	s_add_u32 s40, s40, 0x1800
	s_addc_u32 s41, s41, 0
	global_load_lds_dwordx4 v76, s[40:41]
	s_add_u32 m0, s47, 0x103c0
	s_add_u32 s42, s42, 0x1800
	s_addc_u32 s43, s43, 0
	global_load_lds_dwordx4 v77, s[42:43]
	s_add_u32 m0, s48, 0x103c0
	s_add_u32 s44, s44, 0x1800
	s_addc_u32 s45, s45, 0
	global_load_lds_dwordx4 v78, s[44:45]
	s_waitcnt vmcnt(20)
	ds_write_b128 v81, v[116:119]
	ds_write_b128 v81, v[120:123] offset:1024
	ds_write_b128 v81, v[124:127] offset:2048
	ds_write_b128 v81, v[128:131] offset:3072
	ds_read_b128 v[52:55], v95
	ds_read_b128 v[56:59], v96
	ds_read_b128 v[60:63], v97
	ds_read_b128 v[0:3], v94
	global_load_dwordx4 v[116:119], v64, s[4:5] offset:384
	global_load_dwordx4 v[120:123], v66, s[4:5] offset:384
	global_load_dwordx4 v[124:127], v68, s[4:5] offset:384
	global_load_dwordx4 v[128:131], v70, s[4:5] offset:384
	s_waitcnt vmcnt(13)
	s_waitcnt lgkmcnt(0)
	s_barrier
	ds_read_b128 v[4:7], v84 offset:0
	ds_read_b128 v[8:11], v84 offset:1024
	ds_read_b128 v[12:15], v84 offset:2048
	ds_read_b128 v[16:19], v84 offset:3072
	ds_read_b128 v[20:23], v84 offset:4096
	ds_read_b128 v[24:27], v84 offset:5120
	ds_read_b128 v[28:31], v84 offset:6144
	ds_read_b128 v[32:35], v84 offset:7168
	ds_read_b128 v[36:39], v84 offset:8192
	ds_read_b128 v[40:43], v84 offset:9216
	ds_read_b128 v[44:47], v84 offset:10240
	ds_read_b128 v[48:51], v84 offset:11264
	s_waitcnt lgkmcnt(6)
	v_mfma_f32_32x32x16_f16 a[80:95], v[4:7], v[52:55], 0
	v_mfma_f32_32x32x16_f16 a[64:79], v[8:11], v[52:55], 0
	v_mfma_f32_32x32x16_f16 a[48:63], v[12:15], v[52:55], 0
	s_waitcnt vmcnt(10)
	s_waitcnt lgkmcnt(0)
	s_barrier
	ds_read_b128 v[4:7], v84 offset:12288
	ds_read_b128 v[8:11], v84 offset:13312
	ds_read_b128 v[12:15], v84 offset:14336
	v_mfma_f32_32x32x16_f16 a[32:47], v[16:19], v[52:55], 0
	ds_read_b128 v[16:19], v84 offset:15360
	v_mfma_f32_32x32x16_f16 a[16:31], v[20:23], v[52:55], 0
	ds_read_b128 v[20:23], v84 offset:16384
	v_mfma_f32_32x32x16_f16 a[0:15], v[24:27], v[52:55], 0
	ds_read_b128 v[24:27], v84 offset:17408
	v_mfma_f32_32x32x16_f16 a[80:95], v[28:31], v[56:59], a[80:95]
	s_add_u32 m0, s46, 0x0
	s_add_u32 s40, s40, 0x1800
	s_addc_u32 s41, s41, 0
	global_load_lds_dwordx4 v76, s[40:41]
	v_mfma_f32_32x32x16_f16 a[64:79], v[32:35], v[56:59], a[64:79]
	s_add_u32 m0, s47, 0x0
	s_add_u32 s42, s42, 0x1800
	s_addc_u32 s43, s43, 0
	global_load_lds_dwordx4 v77, s[42:43]
	v_mfma_f32_32x32x16_f16 a[48:63], v[36:39], v[56:59], a[48:63]
	s_add_u32 m0, s48, 0x0
	s_add_u32 s44, s44, 0x1800
	s_addc_u32 s45, s45, 0
	global_load_lds_dwordx4 v78, s[44:45]
	v_mfma_f32_32x32x16_f16 a[32:47], v[40:43], v[56:59], a[32:47]
	v_mfma_f32_32x32x16_f16 a[16:31], v[44:47], v[56:59], a[16:31]
	v_mfma_f32_32x32x16_f16 a[0:15], v[48:51], v[56:59], a[0:15]
	ds_read_b128 v[28:31], v84 offset:18432
	ds_read_b128 v[32:35], v84 offset:19456
	ds_read_b128 v[36:39], v84 offset:20480
	ds_read_b128 v[40:43], v84 offset:21504
	ds_read_b128 v[44:47], v84 offset:22528
	ds_read_b128 v[48:51], v84 offset:23552
	s_waitcnt lgkmcnt(6)
	v_mfma_f32_32x32x16_f16 a[80:95], v[4:7], v[60:63], a[80:95]
	s_waitcnt vmcnt(23)
	ds_write_b128 v81, v[132:135]
	ds_write_b128 v81, v[136:139] offset:1024
	ds_write_b128 v81, v[140:143] offset:2048
	ds_write_b128 v81, v[144:147] offset:3072
	v_mfma_f32_32x32x16_f16 a[64:79], v[8:11], v[60:63], a[64:79]
	ds_read_b128 v[100:103], v95
	ds_read_b128 v[104:107], v96
	ds_read_b128 v[108:111], v97
	ds_read_b128 v[112:115], v94
	v_mfma_f32_32x32x16_f16 a[48:63], v[12:15], v[60:63], a[48:63]
	global_load_dwordx4 v[132:135], v64, s[4:5] offset:512
	global_load_dwordx4 v[136:139], v66, s[4:5] offset:512
	global_load_dwordx4 v[140:143], v68, s[4:5] offset:512
	global_load_dwordx4 v[144:147], v70, s[4:5] offset:512
	s_waitcnt vmcnt(14)
	s_waitcnt lgkmcnt(8)
	s_barrier
	ds_read_b128 v[4:7], v84 offset:54208
	ds_read_b128 v[8:11], v84 offset:55232
	ds_read_b128 v[12:15], v84 offset:56256
	v_mfma_f32_32x32x16_f16 a[32:47], v[16:19], v[60:63], a[32:47]
	ds_read_b128 v[16:19], v84 offset:57280
	v_mfma_f32_32x32x16_f16 a[16:31], v[20:23], v[60:63], a[16:31]
	ds_read_b128 v[20:23], v84 offset:58304
	v_mfma_f32_32x32x16_f16 a[0:15], v[24:27], v[60:63], a[0:15]
	ds_read_b128 v[24:27], v84 offset:59328
	v_mfma_f32_32x32x16_f16 a[80:95], v[28:31], v[0:3], a[80:95]
	s_add_u32 m0, s46, 0x3000
	s_add_u32 s40, s40, 0x1800
	s_addc_u32 s41, s41, 0
	global_load_lds_dwordx4 v76, s[40:41]
	v_mfma_f32_32x32x16_f16 a[64:79], v[32:35], v[0:3], a[64:79]
	s_add_u32 m0, s47, 0x3000
	s_add_u32 s42, s42, 0x1800
	s_addc_u32 s43, s43, 0
	global_load_lds_dwordx4 v77, s[42:43]
	v_mfma_f32_32x32x16_f16 a[48:63], v[36:39], v[0:3], a[48:63]
	s_add_u32 m0, s48, 0x3000
	s_add_u32 s44, s44, 0x1800
	s_addc_u32 s45, s45, 0
	global_load_lds_dwordx4 v78, s[44:45]
	v_mfma_f32_32x32x16_f16 a[32:47], v[40:43], v[0:3], a[32:47]
	v_mfma_f32_32x32x16_f16 a[16:31], v[44:47], v[0:3], a[16:31]
	v_mfma_f32_32x32x16_f16 a[0:15], v[48:51], v[0:3], a[0:15]
	s_waitcnt lgkmcnt(6)
	ds_read_b128 v[28:31], v84 offset:60352
	ds_read_b128 v[32:35], v84 offset:61376
	ds_read_b128 v[36:39], v84 offset:62400
	ds_read_b128 v[40:43], v84 offset:63424
	ds_read_b128 v[44:47], v84 offset:64448
	ds_read_b128 v[48:51], v84 offset:65472
	s_waitcnt lgkmcnt(6)
	v_mfma_f32_32x32x16_f16 a[80:95], v[4:7], v[100:103], a[80:95]
	v_mfma_f32_32x32x16_f16 a[64:79], v[8:11], v[100:103], a[64:79]
	v_mfma_f32_32x32x16_f16 a[48:63], v[12:15], v[100:103], a[48:63]
	s_waitcnt vmcnt(14)
	s_waitcnt lgkmcnt(0)
	s_barrier
	ds_read_b128 v[4:7], v98
	ds_read_b128 v[8:11], v98 offset:1024
	ds_read_b128 v[12:15], v98 offset:2048
	v_mfma_f32_32x32x16_f16 a[32:47], v[16:19], v[100:103], a[32:47]
	ds_read_b128 v[16:19], v98 offset:3072
	v_mfma_f32_32x32x16_f16 a[16:31], v[20:23], v[100:103], a[16:31]
	ds_read_b128 v[20:23], v98 offset:4096
	v_mfma_f32_32x32x16_f16 a[0:15], v[24:27], v[100:103], a[0:15]
	ds_read_b128 v[24:27], v98 offset:5120
	v_mfma_f32_32x32x16_f16 a[80:95], v[28:31], v[104:107], a[80:95]
	s_add_u32 m0, s46, 0xd3c0
	s_add_u32 s40, s40, 0x1800
	s_addc_u32 s41, s41, 0
	global_load_lds_dwordx4 v76, s[40:41]
	v_mfma_f32_32x32x16_f16 a[64:79], v[32:35], v[104:107], a[64:79]
	s_add_u32 m0, s47, 0xd3c0
	s_add_u32 s42, s42, 0x1800
	s_addc_u32 s43, s43, 0
	global_load_lds_dwordx4 v77, s[42:43]
	v_mfma_f32_32x32x16_f16 a[48:63], v[36:39], v[104:107], a[48:63]
	s_add_u32 m0, s48, 0xd3c0
	s_add_u32 s44, s44, 0x1800
	s_addc_u32 s45, s45, 0
	global_load_lds_dwordx4 v78, s[44:45]
	v_mfma_f32_32x32x16_f16 a[32:47], v[40:43], v[104:107], a[32:47]
	v_mfma_f32_32x32x16_f16 a[16:31], v[44:47], v[104:107], a[16:31]
	v_mfma_f32_32x32x16_f16 a[0:15], v[48:51], v[104:107], a[0:15]
	ds_read_b128 v[28:31], v98 offset:6144
	ds_read_b128 v[32:35], v98 offset:7168
	ds_read_b128 v[36:39], v98 offset:8192
	ds_read_b128 v[40:43], v98 offset:9216
	ds_read_b128 v[44:47], v98 offset:10240
	ds_read_b128 v[48:51], v98 offset:11264
	s_waitcnt lgkmcnt(6)
	v_mfma_f32_32x32x16_f16 a[80:95], v[4:7], v[108:111], a[80:95]
	s_waitcnt vmcnt(29)
	ds_write_b128 v81, v[148:151]
	ds_write_b128 v81, v[152:155] offset:1024
	ds_write_b128 v81, v[156:159] offset:2048
	ds_write_b128 v81, v[72:75] offset:3072
	v_mfma_f32_32x32x16_f16 a[64:79], v[8:11], v[108:111], a[64:79]
	ds_read_b128 v[52:55], v95
	ds_read_b128 v[56:59], v96
	ds_read_b128 v[60:63], v97
	ds_read_b128 v[0:3], v94
	v_mfma_f32_32x32x16_f16 a[48:63], v[12:15], v[108:111], a[48:63]
	global_load_dwordx4 v[148:151], v64, s[4:5] offset:640
	global_load_dwordx4 v[152:155], v66, s[4:5] offset:640
	global_load_dwordx4 v[156:159], v68, s[4:5] offset:640
	global_load_dwordx4 v[72:75], v70, s[4:5] offset:640
	s_waitcnt vmcnt(14)
	s_waitcnt lgkmcnt(8)
	s_barrier
	ds_read_b128 v[4:7], v84 offset:0
	ds_read_b128 v[8:11], v84 offset:1024
	ds_read_b128 v[12:15], v84 offset:2048
	v_mfma_f32_32x32x16_f16 a[32:47], v[16:19], v[108:111], a[32:47]
	ds_read_b128 v[16:19], v84 offset:3072
	v_mfma_f32_32x32x16_f16 a[16:31], v[20:23], v[108:111], a[16:31]
	ds_read_b128 v[20:23], v84 offset:4096
	v_mfma_f32_32x32x16_f16 a[0:15], v[24:27], v[108:111], a[0:15]
	ds_read_b128 v[24:27], v84 offset:5120
	v_mfma_f32_32x32x16_f16 a[80:95], v[28:31], v[112:115], a[80:95]
	s_add_u32 m0, s46, 0x103c0
	s_add_u32 s40, s40, 0x1800
	s_addc_u32 s41, s41, 0
	global_load_lds_dwordx4 v76, s[40:41]
	v_mfma_f32_32x32x16_f16 a[64:79], v[32:35], v[112:115], a[64:79]
	s_add_u32 m0, s47, 0x103c0
	s_add_u32 s42, s42, 0x1800
	s_addc_u32 s43, s43, 0
	global_load_lds_dwordx4 v77, s[42:43]
	v_mfma_f32_32x32x16_f16 a[48:63], v[36:39], v[112:115], a[48:63]
	s_add_u32 m0, s48, 0x103c0
	s_add_u32 s44, s44, 0x1800
	s_addc_u32 s45, s45, 0
	global_load_lds_dwordx4 v78, s[44:45]
	v_mfma_f32_32x32x16_f16 a[32:47], v[40:43], v[112:115], a[32:47]
	v_mfma_f32_32x32x16_f16 a[16:31], v[44:47], v[112:115], a[16:31]
	v_mfma_f32_32x32x16_f16 a[0:15], v[48:51], v[112:115], a[0:15]
	s_waitcnt lgkmcnt(6)
	ds_read_b128 v[28:31], v84 offset:6144
	ds_read_b128 v[32:35], v84 offset:7168
	ds_read_b128 v[36:39], v84 offset:8192
	ds_read_b128 v[40:43], v84 offset:9216
	ds_read_b128 v[44:47], v84 offset:10240
	ds_read_b128 v[48:51], v84 offset:11264
	s_waitcnt lgkmcnt(6)
	v_mfma_f32_32x32x16_f16 a[80:95], v[4:7], v[52:55], a[80:95]
	v_mfma_f32_32x32x16_f16 a[64:79], v[8:11], v[52:55], a[64:79]
	v_mfma_f32_32x32x16_f16 a[48:63], v[12:15], v[52:55], a[48:63]
	s_waitcnt vmcnt(10)
	s_waitcnt lgkmcnt(0)
	s_barrier
	ds_read_b128 v[4:7], v84 offset:12288
	ds_read_b128 v[8:11], v84 offset:13312
	ds_read_b128 v[12:15], v84 offset:14336
	v_mfma_f32_32x32x16_f16 a[32:47], v[16:19], v[52:55], a[32:47]
	ds_read_b128 v[16:19], v84 offset:15360
	v_mfma_f32_32x32x16_f16 a[16:31], v[20:23], v[52:55], a[16:31]
	ds_read_b128 v[20:23], v84 offset:16384
	v_mfma_f32_32x32x16_f16 a[0:15], v[24:27], v[52:55], a[0:15]
	ds_read_b128 v[24:27], v84 offset:17408
	v_mfma_f32_32x32x16_f16 a[80:95], v[28:31], v[56:59], a[80:95]
	s_add_u32 m0, s46, 0x0
	s_add_u32 s40, s40, 0x1800
	s_addc_u32 s41, s41, 0
	global_load_lds_dwordx4 v76, s[40:41]
	v_mfma_f32_32x32x16_f16 a[64:79], v[32:35], v[56:59], a[64:79]
	s_add_u32 m0, s47, 0x0
	s_add_u32 s42, s42, 0x1800
	s_addc_u32 s43, s43, 0
	global_load_lds_dwordx4 v77, s[42:43]
	v_mfma_f32_32x32x16_f16 a[48:63], v[36:39], v[56:59], a[48:63]
	s_add_u32 m0, s48, 0x0
	s_add_u32 s44, s44, 0x1800
	s_addc_u32 s45, s45, 0
	global_load_lds_dwordx4 v78, s[44:45]
	v_mfma_f32_32x32x16_f16 a[32:47], v[40:43], v[56:59], a[32:47]
	v_mfma_f32_32x32x16_f16 a[16:31], v[44:47], v[56:59], a[16:31]
	v_mfma_f32_32x32x16_f16 a[0:15], v[48:51], v[56:59], a[0:15]
	ds_read_b128 v[28:31], v84 offset:18432
	ds_read_b128 v[32:35], v84 offset:19456
	ds_read_b128 v[36:39], v84 offset:20480
	ds_read_b128 v[40:43], v84 offset:21504
	ds_read_b128 v[44:47], v84 offset:22528
	ds_read_b128 v[48:51], v84 offset:23552
	s_waitcnt lgkmcnt(6)
	v_mfma_f32_32x32x16_f16 a[80:95], v[4:7], v[60:63], a[80:95]
	s_waitcnt vmcnt(23)
	ds_write_b128 v81, v[116:119]
	ds_write_b128 v81, v[120:123] offset:1024
	ds_write_b128 v81, v[124:127] offset:2048
	ds_write_b128 v81, v[128:131] offset:3072
	v_mfma_f32_32x32x16_f16 a[64:79], v[8:11], v[60:63], a[64:79]
	ds_read_b128 v[100:103], v95
	ds_read_b128 v[104:107], v96
	ds_read_b128 v[108:111], v97
	ds_read_b128 v[112:115], v94
	v_mfma_f32_32x32x16_f16 a[48:63], v[12:15], v[60:63], a[48:63]
	global_load_dwordx4 v[116:119], v64, s[4:5] offset:768
	global_load_dwordx4 v[120:123], v66, s[4:5] offset:768
	global_load_dwordx4 v[124:127], v68, s[4:5] offset:768
	global_load_dwordx4 v[128:131], v70, s[4:5] offset:768
	s_waitcnt vmcnt(14)
	s_waitcnt lgkmcnt(8)
	s_barrier
	ds_read_b128 v[4:7], v84 offset:54208
	ds_read_b128 v[8:11], v84 offset:55232
	ds_read_b128 v[12:15], v84 offset:56256
	v_mfma_f32_32x32x16_f16 a[32:47], v[16:19], v[60:63], a[32:47]
	ds_read_b128 v[16:19], v84 offset:57280
	v_mfma_f32_32x32x16_f16 a[16:31], v[20:23], v[60:63], a[16:31]
	ds_read_b128 v[20:23], v84 offset:58304
	v_mfma_f32_32x32x16_f16 a[0:15], v[24:27], v[60:63], a[0:15]
	ds_read_b128 v[24:27], v84 offset:59328
	v_mfma_f32_32x32x16_f16 a[80:95], v[28:31], v[0:3], a[80:95]
	s_add_u32 m0, s46, 0x3000
	s_add_u32 s40, s40, 0x1800
	s_addc_u32 s41, s41, 0
	global_load_lds_dwordx4 v76, s[40:41]
	v_mfma_f32_32x32x16_f16 a[64:79], v[32:35], v[0:3], a[64:79]
	s_add_u32 m0, s47, 0x3000
	s_add_u32 s42, s42, 0x1800
	s_addc_u32 s43, s43, 0
	global_load_lds_dwordx4 v77, s[42:43]
	v_mfma_f32_32x32x16_f16 a[48:63], v[36:39], v[0:3], a[48:63]
	s_add_u32 m0, s48, 0x3000
	s_add_u32 s44, s44, 0x1800
	s_addc_u32 s45, s45, 0
	global_load_lds_dwordx4 v78, s[44:45]
	v_mfma_f32_32x32x16_f16 a[32:47], v[40:43], v[0:3], a[32:47]
	v_mfma_f32_32x32x16_f16 a[16:31], v[44:47], v[0:3], a[16:31]
	v_mfma_f32_32x32x16_f16 a[0:15], v[48:51], v[0:3], a[0:15]
	s_waitcnt lgkmcnt(6)
	ds_read_b128 v[28:31], v84 offset:60352
	ds_read_b128 v[32:35], v84 offset:61376
	ds_read_b128 v[36:39], v84 offset:62400
	ds_read_b128 v[40:43], v84 offset:63424
	ds_read_b128 v[44:47], v84 offset:64448
	ds_read_b128 v[48:51], v84 offset:65472
	s_waitcnt lgkmcnt(6)
	v_mfma_f32_32x32x16_f16 a[80:95], v[4:7], v[100:103], a[80:95]
	v_mfma_f32_32x32x16_f16 a[64:79], v[8:11], v[100:103], a[64:79]
	v_mfma_f32_32x32x16_f16 a[48:63], v[12:15], v[100:103], a[48:63]
	s_waitcnt vmcnt(10)
	s_waitcnt lgkmcnt(0)
	s_barrier
	ds_read_b128 v[4:7], v98
	ds_read_b128 v[8:11], v98 offset:1024
	ds_read_b128 v[12:15], v98 offset:2048
	v_mfma_f32_32x32x16_f16 a[32:47], v[16:19], v[100:103], a[32:47]
	ds_read_b128 v[16:19], v98 offset:3072
	v_mfma_f32_32x32x16_f16 a[16:31], v[20:23], v[100:103], a[16:31]
	ds_read_b128 v[20:23], v98 offset:4096
	v_mfma_f32_32x32x16_f16 a[0:15], v[24:27], v[100:103], a[0:15]
	ds_read_b128 v[24:27], v98 offset:5120
	v_mfma_f32_32x32x16_f16 a[80:95], v[28:31], v[104:107], a[80:95]
	s_add_u32 m0, s46, 0xd3c0
	s_add_u32 s40, s40, 0x1800
	s_addc_u32 s41, s41, 0
	global_load_lds_dwordx4 v76, s[40:41]
	v_mfma_f32_32x32x16_f16 a[64:79], v[32:35], v[104:107], a[64:79]
	s_add_u32 m0, s47, 0xd3c0
	s_add_u32 s42, s42, 0x1800
	s_addc_u32 s43, s43, 0
	global_load_lds_dwordx4 v77, s[42:43]
	v_mfma_f32_32x32x16_f16 a[48:63], v[36:39], v[104:107], a[48:63]
	s_add_u32 m0, s48, 0xd3c0
	s_add_u32 s44, s44, 0x1800
	s_addc_u32 s45, s45, 0
	global_load_lds_dwordx4 v78, s[44:45]
	v_mfma_f32_32x32x16_f16 a[32:47], v[40:43], v[104:107], a[32:47]
	v_mfma_f32_32x32x16_f16 a[16:31], v[44:47], v[104:107], a[16:31]
	v_mfma_f32_32x32x16_f16 a[0:15], v[48:51], v[104:107], a[0:15]
	ds_read_b128 v[28:31], v98 offset:6144
	ds_read_b128 v[32:35], v98 offset:7168
	ds_read_b128 v[36:39], v98 offset:8192
	ds_read_b128 v[40:43], v98 offset:9216
	ds_read_b128 v[44:47], v98 offset:10240
	ds_read_b128 v[48:51], v98 offset:11264
	s_waitcnt lgkmcnt(6)
	v_mfma_f32_32x32x16_f16 a[80:95], v[4:7], v[108:111], a[80:95]
	s_waitcnt vmcnt(26)
	ds_write_b128 v81, v[132:135]
	ds_write_b128 v81, v[136:139] offset:1024
	ds_write_b128 v81, v[140:143] offset:2048
	ds_write_b128 v81, v[144:147] offset:3072
	v_mfma_f32_32x32x16_f16 a[64:79], v[8:11], v[108:111], a[64:79]
	ds_read_b128 v[52:55], v95
	ds_read_b128 v[56:59], v96
	ds_read_b128 v[60:63], v97
	ds_read_b128 v[0:3], v94
	v_mfma_f32_32x32x16_f16 a[48:63], v[12:15], v[108:111], a[48:63]
	global_load_dwordx4 v[132:135], v64, s[4:5] offset:896
	global_load_dwordx4 v[136:139], v66, s[4:5] offset:896
	global_load_dwordx4 v[140:143], v68, s[4:5] offset:896
	global_load_dwordx4 v[144:147], v70, s[4:5] offset:896
	s_waitcnt vmcnt(14)
	s_waitcnt lgkmcnt(8)
	s_barrier
	ds_read_b128 v[4:7], v84 offset:0
	ds_read_b128 v[8:11], v84 offset:1024
	ds_read_b128 v[12:15], v84 offset:2048
	v_mfma_f32_32x32x16_f16 a[32:47], v[16:19], v[108:111], a[32:47]
	ds_read_b128 v[16:19], v84 offset:3072
	v_mfma_f32_32x32x16_f16 a[16:31], v[20:23], v[108:111], a[16:31]
	ds_read_b128 v[20:23], v84 offset:4096
	v_mfma_f32_32x32x16_f16 a[0:15], v[24:27], v[108:111], a[0:15]
	ds_read_b128 v[24:27], v84 offset:5120
	v_mfma_f32_32x32x16_f16 a[80:95], v[28:31], v[112:115], a[80:95]
	s_add_u32 m0, s46, 0x103c0
	s_add_u32 s40, s40, 0x1800
	s_addc_u32 s41, s41, 0
	global_load_lds_dwordx4 v76, s[40:41]
	v_mfma_f32_32x32x16_f16 a[64:79], v[32:35], v[112:115], a[64:79]
	s_add_u32 m0, s47, 0x103c0
	s_add_u32 s42, s42, 0x1800
	s_addc_u32 s43, s43, 0
	global_load_lds_dwordx4 v77, s[42:43]
	v_mfma_f32_32x32x16_f16 a[48:63], v[36:39], v[112:115], a[48:63]
	s_add_u32 m0, s48, 0x103c0
	s_add_u32 s44, s44, 0x1800
	s_addc_u32 s45, s45, 0
	global_load_lds_dwordx4 v78, s[44:45]
	v_mfma_f32_32x32x16_f16 a[32:47], v[40:43], v[112:115], a[32:47]
	v_mfma_f32_32x32x16_f16 a[16:31], v[44:47], v[112:115], a[16:31]
	v_mfma_f32_32x32x16_f16 a[0:15], v[48:51], v[112:115], a[0:15]
	s_waitcnt lgkmcnt(6)
	ds_read_b128 v[28:31], v84 offset:6144
	ds_read_b128 v[32:35], v84 offset:7168
	ds_read_b128 v[36:39], v84 offset:8192
	ds_read_b128 v[40:43], v84 offset:9216
	ds_read_b128 v[44:47], v84 offset:10240
	ds_read_b128 v[48:51], v84 offset:11264
	s_waitcnt lgkmcnt(6)
	v_mfma_f32_32x32x16_f16 a[80:95], v[4:7], v[52:55], a[80:95]
	v_mfma_f32_32x32x16_f16 a[64:79], v[8:11], v[52:55], a[64:79]
	v_mfma_f32_32x32x16_f16 a[48:63], v[12:15], v[52:55], a[48:63]
	s_waitcnt vmcnt(10)
	s_waitcnt lgkmcnt(0)
	s_barrier
	ds_read_b128 v[4:7], v84 offset:12288
	ds_read_b128 v[8:11], v84 offset:13312
	ds_read_b128 v[12:15], v84 offset:14336
	v_mfma_f32_32x32x16_f16 a[32:47], v[16:19], v[52:55], a[32:47]
	ds_read_b128 v[16:19], v84 offset:15360
	v_mfma_f32_32x32x16_f16 a[16:31], v[20:23], v[52:55], a[16:31]
	ds_read_b128 v[20:23], v84 offset:16384
	v_mfma_f32_32x32x16_f16 a[0:15], v[24:27], v[52:55], a[0:15]
	ds_read_b128 v[24:27], v84 offset:17408
	v_mfma_f32_32x32x16_f16 a[80:95], v[28:31], v[56:59], a[80:95]
	s_add_u32 m0, s46, 0x0
	s_add_u32 s40, s40, 0x1800
	s_addc_u32 s41, s41, 0
	global_load_lds_dwordx4 v76, s[40:41]
	v_mfma_f32_32x32x16_f16 a[64:79], v[32:35], v[56:59], a[64:79]
	s_add_u32 m0, s47, 0x0
	s_add_u32 s42, s42, 0x1800
	s_addc_u32 s43, s43, 0
	global_load_lds_dwordx4 v77, s[42:43]
	v_mfma_f32_32x32x16_f16 a[48:63], v[36:39], v[56:59], a[48:63]
	s_add_u32 m0, s48, 0x0
	s_add_u32 s44, s44, 0x1800
	s_addc_u32 s45, s45, 0
	global_load_lds_dwordx4 v78, s[44:45]
	v_mfma_f32_32x32x16_f16 a[32:47], v[40:43], v[56:59], a[32:47]
	v_mfma_f32_32x32x16_f16 a[16:31], v[44:47], v[56:59], a[16:31]
	v_mfma_f32_32x32x16_f16 a[0:15], v[48:51], v[56:59], a[0:15]
	ds_read_b128 v[28:31], v84 offset:18432
	ds_read_b128 v[32:35], v84 offset:19456
	ds_read_b128 v[36:39], v84 offset:20480
	ds_read_b128 v[40:43], v84 offset:21504
	ds_read_b128 v[44:47], v84 offset:22528
	ds_read_b128 v[48:51], v84 offset:23552
	s_waitcnt lgkmcnt(6)
	v_mfma_f32_32x32x16_f16 a[80:95], v[4:7], v[60:63], a[80:95]
	s_waitcnt vmcnt(26)
	ds_write_b128 v81, v[148:151]
	ds_write_b128 v81, v[152:155] offset:1024
	ds_write_b128 v81, v[156:159] offset:2048
	ds_write_b128 v81, v[72:75] offset:3072
	v_mfma_f32_32x32x16_f16 a[64:79], v[8:11], v[60:63], a[64:79]
	ds_read_b128 v[100:103], v95
	ds_read_b128 v[104:107], v96
	ds_read_b128 v[108:111], v97
	ds_read_b128 v[112:115], v94
	v_mfma_f32_32x32x16_f16 a[48:63], v[12:15], v[60:63], a[48:63]
	global_load_dwordx4 v[148:151], v64, s[4:5] offset:1024
	global_load_dwordx4 v[152:155], v66, s[4:5] offset:1024
	global_load_dwordx4 v[156:159], v68, s[4:5] offset:1024
	global_load_dwordx4 v[72:75], v70, s[4:5] offset:1024
	s_waitcnt vmcnt(14)
	s_waitcnt lgkmcnt(8)
	s_barrier
	ds_read_b128 v[4:7], v84 offset:54208
	ds_read_b128 v[8:11], v84 offset:55232
	ds_read_b128 v[12:15], v84 offset:56256
	v_mfma_f32_32x32x16_f16 a[32:47], v[16:19], v[60:63], a[32:47]
	ds_read_b128 v[16:19], v84 offset:57280
	v_mfma_f32_32x32x16_f16 a[16:31], v[20:23], v[60:63], a[16:31]
	ds_read_b128 v[20:23], v84 offset:58304
	v_mfma_f32_32x32x16_f16 a[0:15], v[24:27], v[60:63], a[0:15]
	ds_read_b128 v[24:27], v84 offset:59328
	v_mfma_f32_32x32x16_f16 a[80:95], v[28:31], v[0:3], a[80:95]
	s_add_u32 m0, s46, 0x3000
	s_add_u32 s40, s40, 0x1800
	s_addc_u32 s41, s41, 0
	global_load_lds_dwordx4 v76, s[40:41]
	v_mfma_f32_32x32x16_f16 a[64:79], v[32:35], v[0:3], a[64:79]
	s_add_u32 m0, s47, 0x3000
	s_add_u32 s42, s42, 0x1800
	s_addc_u32 s43, s43, 0
	global_load_lds_dwordx4 v77, s[42:43]
	v_mfma_f32_32x32x16_f16 a[48:63], v[36:39], v[0:3], a[48:63]
	s_add_u32 m0, s48, 0x3000
	s_add_u32 s44, s44, 0x1800
	s_addc_u32 s45, s45, 0
	global_load_lds_dwordx4 v78, s[44:45]
	v_mfma_f32_32x32x16_f16 a[32:47], v[40:43], v[0:3], a[32:47]
	v_mfma_f32_32x32x16_f16 a[16:31], v[44:47], v[0:3], a[16:31]
	v_mfma_f32_32x32x16_f16 a[0:15], v[48:51], v[0:3], a[0:15]
	s_waitcnt lgkmcnt(6)
	ds_read_b128 v[28:31], v84 offset:60352
	ds_read_b128 v[32:35], v84 offset:61376
	ds_read_b128 v[36:39], v84 offset:62400
	ds_read_b128 v[40:43], v84 offset:63424
	ds_read_b128 v[44:47], v84 offset:64448
	ds_read_b128 v[48:51], v84 offset:65472
	s_waitcnt lgkmcnt(6)
	v_mfma_f32_32x32x16_f16 a[80:95], v[4:7], v[100:103], a[80:95]
	v_mfma_f32_32x32x16_f16 a[64:79], v[8:11], v[100:103], a[64:79]
	v_mfma_f32_32x32x16_f16 a[48:63], v[12:15], v[100:103], a[48:63]
	s_waitcnt vmcnt(10)
	s_waitcnt lgkmcnt(0)
	s_barrier
	ds_read_b128 v[4:7], v98
	ds_read_b128 v[8:11], v98 offset:1024
	ds_read_b128 v[12:15], v98 offset:2048
	v_mfma_f32_32x32x16_f16 a[32:47], v[16:19], v[100:103], a[32:47]
	ds_read_b128 v[16:19], v98 offset:3072
	v_mfma_f32_32x32x16_f16 a[16:31], v[20:23], v[100:103], a[16:31]
	ds_read_b128 v[20:23], v98 offset:4096
	v_mfma_f32_32x32x16_f16 a[0:15], v[24:27], v[100:103], a[0:15]
	ds_read_b128 v[24:27], v98 offset:5120
	v_mfma_f32_32x32x16_f16 a[80:95], v[28:31], v[104:107], a[80:95]
	s_add_u32 m0, s46, 0xd3c0
	s_add_u32 s40, s40, 0x1800
	s_addc_u32 s41, s41, 0
	global_load_lds_dwordx4 v76, s[40:41]
	v_mfma_f32_32x32x16_f16 a[64:79], v[32:35], v[104:107], a[64:79]
	s_add_u32 m0, s47, 0xd3c0
	s_add_u32 s42, s42, 0x1800
	s_addc_u32 s43, s43, 0
	global_load_lds_dwordx4 v77, s[42:43]
	v_mfma_f32_32x32x16_f16 a[48:63], v[36:39], v[104:107], a[48:63]
	s_add_u32 m0, s48, 0xd3c0
	s_add_u32 s44, s44, 0x1800
	s_addc_u32 s45, s45, 0
	global_load_lds_dwordx4 v78, s[44:45]
	v_mfma_f32_32x32x16_f16 a[32:47], v[40:43], v[104:107], a[32:47]
	v_mfma_f32_32x32x16_f16 a[16:31], v[44:47], v[104:107], a[16:31]
	v_mfma_f32_32x32x16_f16 a[0:15], v[48:51], v[104:107], a[0:15]
	ds_read_b128 v[28:31], v98 offset:6144
	ds_read_b128 v[32:35], v98 offset:7168
	ds_read_b128 v[36:39], v98 offset:8192
	ds_read_b128 v[40:43], v98 offset:9216
	ds_read_b128 v[44:47], v98 offset:10240
	ds_read_b128 v[48:51], v98 offset:11264
	s_waitcnt lgkmcnt(6)
	v_mfma_f32_32x32x16_f16 a[80:95], v[4:7], v[108:111], a[80:95]
	s_waitcnt vmcnt(26)
	ds_write_b128 v81, v[116:119]
	ds_write_b128 v81, v[120:123] offset:1024
	ds_write_b128 v81, v[124:127] offset:2048
	ds_write_b128 v81, v[128:131] offset:3072
	v_mfma_f32_32x32x16_f16 a[64:79], v[8:11], v[108:111], a[64:79]
	ds_read_b128 v[52:55], v95
	ds_read_b128 v[56:59], v96
	ds_read_b128 v[60:63], v97
	ds_read_b128 v[0:3], v94
	v_mfma_f32_32x32x16_f16 a[48:63], v[12:15], v[108:111], a[48:63]
	global_load_dwordx4 v[116:119], v64, s[4:5] offset:1152
	global_load_dwordx4 v[120:123], v66, s[4:5] offset:1152
	global_load_dwordx4 v[124:127], v68, s[4:5] offset:1152
	global_load_dwordx4 v[128:131], v70, s[4:5] offset:1152
	s_waitcnt vmcnt(14)
	s_waitcnt lgkmcnt(8)
	s_barrier
	ds_read_b128 v[4:7], v84 offset:0
	ds_read_b128 v[8:11], v84 offset:1024
	ds_read_b128 v[12:15], v84 offset:2048
	v_mfma_f32_32x32x16_f16 a[32:47], v[16:19], v[108:111], a[32:47]
	ds_read_b128 v[16:19], v84 offset:3072
	v_mfma_f32_32x32x16_f16 a[16:31], v[20:23], v[108:111], a[16:31]
	ds_read_b128 v[20:23], v84 offset:4096
	v_mfma_f32_32x32x16_f16 a[0:15], v[24:27], v[108:111], a[0:15]
	ds_read_b128 v[24:27], v84 offset:5120
	v_mfma_f32_32x32x16_f16 a[80:95], v[28:31], v[112:115], a[80:95]
	s_add_u32 m0, s46, 0x103c0
	s_add_u32 s40, s40, 0x1800
	s_addc_u32 s41, s41, 0
	global_load_lds_dwordx4 v76, s[40:41]
	v_mfma_f32_32x32x16_f16 a[64:79], v[32:35], v[112:115], a[64:79]
	s_add_u32 m0, s47, 0x103c0
	s_add_u32 s42, s42, 0x1800
	s_addc_u32 s43, s43, 0
	global_load_lds_dwordx4 v77, s[42:43]
	v_mfma_f32_32x32x16_f16 a[48:63], v[36:39], v[112:115], a[48:63]
	s_add_u32 m0, s48, 0x103c0
	s_add_u32 s44, s44, 0x1800
	s_addc_u32 s45, s45, 0
	global_load_lds_dwordx4 v78, s[44:45]
	v_mfma_f32_32x32x16_f16 a[32:47], v[40:43], v[112:115], a[32:47]
	v_mfma_f32_32x32x16_f16 a[16:31], v[44:47], v[112:115], a[16:31]
	v_mfma_f32_32x32x16_f16 a[0:15], v[48:51], v[112:115], a[0:15]
	s_waitcnt lgkmcnt(6)
	ds_read_b128 v[28:31], v84 offset:6144
	ds_read_b128 v[32:35], v84 offset:7168
	ds_read_b128 v[36:39], v84 offset:8192
	ds_read_b128 v[40:43], v84 offset:9216
	ds_read_b128 v[44:47], v84 offset:10240
	ds_read_b128 v[48:51], v84 offset:11264
	s_waitcnt lgkmcnt(6)
	v_mfma_f32_32x32x16_f16 a[80:95], v[4:7], v[52:55], a[80:95]
	v_mfma_f32_32x32x16_f16 a[64:79], v[8:11], v[52:55], a[64:79]
	v_mfma_f32_32x32x16_f16 a[48:63], v[12:15], v[52:55], a[48:63]
	s_waitcnt vmcnt(10)
	s_waitcnt lgkmcnt(0)
	s_barrier
	ds_read_b128 v[4:7], v84 offset:12288
	ds_read_b128 v[8:11], v84 offset:13312
	ds_read_b128 v[12:15], v84 offset:14336
	v_mfma_f32_32x32x16_f16 a[32:47], v[16:19], v[52:55], a[32:47]
	ds_read_b128 v[16:19], v84 offset:15360
	v_mfma_f32_32x32x16_f16 a[16:31], v[20:23], v[52:55], a[16:31]
	ds_read_b128 v[20:23], v84 offset:16384
	v_mfma_f32_32x32x16_f16 a[0:15], v[24:27], v[52:55], a[0:15]
	ds_read_b128 v[24:27], v84 offset:17408
	v_mfma_f32_32x32x16_f16 a[80:95], v[28:31], v[56:59], a[80:95]
	s_add_u32 m0, s46, 0x0
	s_add_u32 s40, s40, 0x1800
	s_addc_u32 s41, s41, 0
	global_load_lds_dwordx4 v76, s[40:41]
	v_mfma_f32_32x32x16_f16 a[64:79], v[32:35], v[56:59], a[64:79]
	s_add_u32 m0, s47, 0x0
	s_add_u32 s42, s42, 0x1800
	s_addc_u32 s43, s43, 0
	global_load_lds_dwordx4 v77, s[42:43]
	v_mfma_f32_32x32x16_f16 a[48:63], v[36:39], v[56:59], a[48:63]
	s_add_u32 m0, s48, 0x0
	s_add_u32 s44, s44, 0x1800
	s_addc_u32 s45, s45, 0
	global_load_lds_dwordx4 v78, s[44:45]
	v_mfma_f32_32x32x16_f16 a[32:47], v[40:43], v[56:59], a[32:47]
	v_mfma_f32_32x32x16_f16 a[16:31], v[44:47], v[56:59], a[16:31]
	v_mfma_f32_32x32x16_f16 a[0:15], v[48:51], v[56:59], a[0:15]
	ds_read_b128 v[28:31], v84 offset:18432
	ds_read_b128 v[32:35], v84 offset:19456
	ds_read_b128 v[36:39], v84 offset:20480
	ds_read_b128 v[40:43], v84 offset:21504
	ds_read_b128 v[44:47], v84 offset:22528
	ds_read_b128 v[48:51], v84 offset:23552
	s_waitcnt lgkmcnt(6)
	v_mfma_f32_32x32x16_f16 a[80:95], v[4:7], v[60:63], a[80:95]
	s_waitcnt vmcnt(26)
	ds_write_b128 v81, v[132:135]
	ds_write_b128 v81, v[136:139] offset:1024
	ds_write_b128 v81, v[140:143] offset:2048
	ds_write_b128 v81, v[144:147] offset:3072
	v_mfma_f32_32x32x16_f16 a[64:79], v[8:11], v[60:63], a[64:79]
	ds_read_b128 v[100:103], v95
	ds_read_b128 v[104:107], v96
	ds_read_b128 v[108:111], v97
	ds_read_b128 v[112:115], v94
	v_mfma_f32_32x32x16_f16 a[48:63], v[12:15], v[60:63], a[48:63]
	global_load_dwordx4 v[132:135], v64, s[4:5] offset:1280
	global_load_dwordx4 v[136:139], v66, s[4:5] offset:1280
	global_load_dwordx4 v[140:143], v68, s[4:5] offset:1280
	global_load_dwordx4 v[144:147], v70, s[4:5] offset:1280
	s_waitcnt vmcnt(14)
	s_waitcnt lgkmcnt(8)
	s_barrier
	ds_read_b128 v[4:7], v84 offset:54208
	ds_read_b128 v[8:11], v84 offset:55232
	ds_read_b128 v[12:15], v84 offset:56256
	v_mfma_f32_32x32x16_f16 a[32:47], v[16:19], v[60:63], a[32:47]
	ds_read_b128 v[16:19], v84 offset:57280
	v_mfma_f32_32x32x16_f16 a[16:31], v[20:23], v[60:63], a[16:31]
	ds_read_b128 v[20:23], v84 offset:58304
	v_mfma_f32_32x32x16_f16 a[0:15], v[24:27], v[60:63], a[0:15]
	ds_read_b128 v[24:27], v84 offset:59328
	v_mfma_f32_32x32x16_f16 a[80:95], v[28:31], v[0:3], a[80:95]
	s_add_u32 m0, s46, 0x3000
	s_add_u32 s40, s40, 0x1800
	s_addc_u32 s41, s41, 0
	global_load_lds_dwordx4 v76, s[40:41]
	v_mfma_f32_32x32x16_f16 a[64:79], v[32:35], v[0:3], a[64:79]
	s_add_u32 m0, s47, 0x3000
	s_add_u32 s42, s42, 0x1800
	s_addc_u32 s43, s43, 0
	global_load_lds_dwordx4 v77, s[42:43]
	v_mfma_f32_32x32x16_f16 a[48:63], v[36:39], v[0:3], a[48:63]
	s_add_u32 m0, s48, 0x3000
	s_add_u32 s44, s44, 0x1800
	s_addc_u32 s45, s45, 0
	global_load_lds_dwordx4 v78, s[44:45]
	v_mfma_f32_32x32x16_f16 a[32:47], v[40:43], v[0:3], a[32:47]
	v_mfma_f32_32x32x16_f16 a[16:31], v[44:47], v[0:3], a[16:31]
	v_mfma_f32_32x32x16_f16 a[0:15], v[48:51], v[0:3], a[0:15]
	s_waitcnt lgkmcnt(6)
	ds_read_b128 v[28:31], v84 offset:60352
	ds_read_b128 v[32:35], v84 offset:61376
	ds_read_b128 v[36:39], v84 offset:62400
	ds_read_b128 v[40:43], v84 offset:63424
	ds_read_b128 v[44:47], v84 offset:64448
	ds_read_b128 v[48:51], v84 offset:65472
	s_waitcnt lgkmcnt(6)
	v_mfma_f32_32x32x16_f16 a[80:95], v[4:7], v[100:103], a[80:95]
	v_mfma_f32_32x32x16_f16 a[64:79], v[8:11], v[100:103], a[64:79]
	v_mfma_f32_32x32x16_f16 a[48:63], v[12:15], v[100:103], a[48:63]
	s_waitcnt vmcnt(10)
	s_waitcnt lgkmcnt(0)
	s_barrier
	ds_read_b128 v[4:7], v98
	ds_read_b128 v[8:11], v98 offset:1024
	ds_read_b128 v[12:15], v98 offset:2048
	v_mfma_f32_32x32x16_f16 a[32:47], v[16:19], v[100:103], a[32:47]
	ds_read_b128 v[16:19], v98 offset:3072
	v_mfma_f32_32x32x16_f16 a[16:31], v[20:23], v[100:103], a[16:31]
	ds_read_b128 v[20:23], v98 offset:4096
	v_mfma_f32_32x32x16_f16 a[0:15], v[24:27], v[100:103], a[0:15]
	ds_read_b128 v[24:27], v98 offset:5120
	v_mfma_f32_32x32x16_f16 a[80:95], v[28:31], v[104:107], a[80:95]
	s_add_u32 m0, s46, 0xd3c0
	s_add_u32 s40, s40, 0x1800
	s_addc_u32 s41, s41, 0
	global_load_lds_dwordx4 v76, s[40:41]
	v_mfma_f32_32x32x16_f16 a[64:79], v[32:35], v[104:107], a[64:79]
	s_add_u32 m0, s47, 0xd3c0
	s_add_u32 s42, s42, 0x1800
	s_addc_u32 s43, s43, 0
	global_load_lds_dwordx4 v77, s[42:43]
	v_mfma_f32_32x32x16_f16 a[48:63], v[36:39], v[104:107], a[48:63]
	s_add_u32 m0, s48, 0xd3c0
	s_add_u32 s44, s44, 0x1800
	s_addc_u32 s45, s45, 0
	global_load_lds_dwordx4 v78, s[44:45]
	v_mfma_f32_32x32x16_f16 a[32:47], v[40:43], v[104:107], a[32:47]
	v_mfma_f32_32x32x16_f16 a[16:31], v[44:47], v[104:107], a[16:31]
	v_mfma_f32_32x32x16_f16 a[0:15], v[48:51], v[104:107], a[0:15]
	ds_read_b128 v[28:31], v98 offset:6144
	ds_read_b128 v[32:35], v98 offset:7168
	ds_read_b128 v[36:39], v98 offset:8192
	ds_read_b128 v[40:43], v98 offset:9216
	ds_read_b128 v[44:47], v98 offset:10240
	ds_read_b128 v[48:51], v98 offset:11264
	s_waitcnt lgkmcnt(6)
	v_mfma_f32_32x32x16_f16 a[80:95], v[4:7], v[108:111], a[80:95]
	s_waitcnt vmcnt(26)
	ds_write_b128 v81, v[148:151]
	ds_write_b128 v81, v[152:155] offset:1024
	ds_write_b128 v81, v[156:159] offset:2048
	ds_write_b128 v81, v[72:75] offset:3072
	v_mfma_f32_32x32x16_f16 a[64:79], v[8:11], v[108:111], a[64:79]
	ds_read_b128 v[52:55], v95
	ds_read_b128 v[56:59], v96
	ds_read_b128 v[60:63], v97
	ds_read_b128 v[0:3], v94
	v_mfma_f32_32x32x16_f16 a[48:63], v[12:15], v[108:111], a[48:63]
	global_load_dwordx4 v[148:151], v64, s[4:5] offset:1408
	global_load_dwordx4 v[152:155], v66, s[4:5] offset:1408
	global_load_dwordx4 v[156:159], v68, s[4:5] offset:1408
	global_load_dwordx4 v[72:75], v70, s[4:5] offset:1408
	s_waitcnt vmcnt(14)
	s_waitcnt lgkmcnt(8)
	s_barrier
	ds_read_b128 v[4:7], v84 offset:0
	ds_read_b128 v[8:11], v84 offset:1024
	ds_read_b128 v[12:15], v84 offset:2048
	v_mfma_f32_32x32x16_f16 a[32:47], v[16:19], v[108:111], a[32:47]
	ds_read_b128 v[16:19], v84 offset:3072
	v_mfma_f32_32x32x16_f16 a[16:31], v[20:23], v[108:111], a[16:31]
	ds_read_b128 v[20:23], v84 offset:4096
	v_mfma_f32_32x32x16_f16 a[0:15], v[24:27], v[108:111], a[0:15]
	ds_read_b128 v[24:27], v84 offset:5120
	v_mfma_f32_32x32x16_f16 a[80:95], v[28:31], v[112:115], a[80:95]
	s_add_u32 m0, s46, 0x103c0
	s_add_u32 s40, s40, 0x1800
	s_addc_u32 s41, s41, 0
	global_load_lds_dwordx4 v76, s[40:41]
	v_mfma_f32_32x32x16_f16 a[64:79], v[32:35], v[112:115], a[64:79]
	s_add_u32 m0, s47, 0x103c0
	s_add_u32 s42, s42, 0x1800
	s_addc_u32 s43, s43, 0
	global_load_lds_dwordx4 v77, s[42:43]
	v_mfma_f32_32x32x16_f16 a[48:63], v[36:39], v[112:115], a[48:63]
	s_add_u32 m0, s48, 0x103c0
	s_add_u32 s44, s44, 0x1800
	s_addc_u32 s45, s45, 0
	global_load_lds_dwordx4 v78, s[44:45]
	v_mfma_f32_32x32x16_f16 a[32:47], v[40:43], v[112:115], a[32:47]
	v_mfma_f32_32x32x16_f16 a[16:31], v[44:47], v[112:115], a[16:31]
	v_mfma_f32_32x32x16_f16 a[0:15], v[48:51], v[112:115], a[0:15]
	s_waitcnt lgkmcnt(6)
	ds_read_b128 v[28:31], v84 offset:6144
	ds_read_b128 v[32:35], v84 offset:7168
	ds_read_b128 v[36:39], v84 offset:8192
	ds_read_b128 v[40:43], v84 offset:9216
	ds_read_b128 v[44:47], v84 offset:10240
	ds_read_b128 v[48:51], v84 offset:11264
	s_waitcnt lgkmcnt(6)
	v_mfma_f32_32x32x16_f16 a[80:95], v[4:7], v[52:55], a[80:95]
	v_mfma_f32_32x32x16_f16 a[64:79], v[8:11], v[52:55], a[64:79]
	v_mfma_f32_32x32x16_f16 a[48:63], v[12:15], v[52:55], a[48:63]
	s_waitcnt vmcnt(10)
	s_waitcnt lgkmcnt(0)
	s_barrier
	ds_read_b128 v[4:7], v84 offset:12288
	ds_read_b128 v[8:11], v84 offset:13312
	ds_read_b128 v[12:15], v84 offset:14336
	v_mfma_f32_32x32x16_f16 a[32:47], v[16:19], v[52:55], a[32:47]
	ds_read_b128 v[16:19], v84 offset:15360
	v_mfma_f32_32x32x16_f16 a[16:31], v[20:23], v[52:55], a[16:31]
	ds_read_b128 v[20:23], v84 offset:16384
	v_mfma_f32_32x32x16_f16 a[0:15], v[24:27], v[52:55], a[0:15]
	ds_read_b128 v[24:27], v84 offset:17408
	v_mfma_f32_32x32x16_f16 a[80:95], v[28:31], v[56:59], a[80:95]
	s_add_u32 m0, s46, 0x0
	s_add_u32 s40, s40, 0x1800
	s_addc_u32 s41, s41, 0
	global_load_lds_dwordx4 v76, s[40:41]
	v_mfma_f32_32x32x16_f16 a[64:79], v[32:35], v[56:59], a[64:79]
	s_add_u32 m0, s47, 0x0
	s_add_u32 s42, s42, 0x1800
	s_addc_u32 s43, s43, 0
	global_load_lds_dwordx4 v77, s[42:43]
	v_mfma_f32_32x32x16_f16 a[48:63], v[36:39], v[56:59], a[48:63]
	s_add_u32 m0, s48, 0x0
	s_add_u32 s44, s44, 0x1800
	s_addc_u32 s45, s45, 0
	global_load_lds_dwordx4 v78, s[44:45]
	v_mfma_f32_32x32x16_f16 a[32:47], v[40:43], v[56:59], a[32:47]
	v_mfma_f32_32x32x16_f16 a[16:31], v[44:47], v[56:59], a[16:31]
	v_mfma_f32_32x32x16_f16 a[0:15], v[48:51], v[56:59], a[0:15]
	ds_read_b128 v[28:31], v84 offset:18432
	ds_read_b128 v[32:35], v84 offset:19456
	ds_read_b128 v[36:39], v84 offset:20480
	ds_read_b128 v[40:43], v84 offset:21504
	ds_read_b128 v[44:47], v84 offset:22528
	ds_read_b128 v[48:51], v84 offset:23552
	s_waitcnt lgkmcnt(6)
	v_mfma_f32_32x32x16_f16 a[80:95], v[4:7], v[60:63], a[80:95]
	s_waitcnt vmcnt(26)
	ds_write_b128 v81, v[116:119]
	ds_write_b128 v81, v[120:123] offset:1024
	ds_write_b128 v81, v[124:127] offset:2048
	ds_write_b128 v81, v[128:131] offset:3072
	v_mfma_f32_32x32x16_f16 a[64:79], v[8:11], v[60:63], a[64:79]
	ds_read_b128 v[100:103], v95
	ds_read_b128 v[104:107], v96
	ds_read_b128 v[108:111], v97
	ds_read_b128 v[112:115], v94
	v_mfma_f32_32x32x16_f16 a[48:63], v[12:15], v[60:63], a[48:63]
	global_load_dwordx4 v[116:119], v64, s[4:5] offset:1440
	global_load_dwordx4 v[120:123], v66, s[4:5] offset:1440
	global_load_dwordx4 v[124:127], v68, s[4:5] offset:1440
	global_load_dwordx4 v[128:131], v70, s[4:5] offset:1440
	s_waitcnt vmcnt(14)
	s_waitcnt lgkmcnt(8)
	s_barrier
	ds_read_b128 v[4:7], v84 offset:54208
	ds_read_b128 v[8:11], v84 offset:55232
	ds_read_b128 v[12:15], v84 offset:56256
	v_mfma_f32_32x32x16_f16 a[32:47], v[16:19], v[60:63], a[32:47]
	ds_read_b128 v[16:19], v84 offset:57280
	v_mfma_f32_32x32x16_f16 a[16:31], v[20:23], v[60:63], a[16:31]
	ds_read_b128 v[20:23], v84 offset:58304
	v_mfma_f32_32x32x16_f16 a[0:15], v[24:27], v[60:63], a[0:15]
	ds_read_b128 v[24:27], v84 offset:59328
	v_mfma_f32_32x32x16_f16 a[80:95], v[28:31], v[0:3], a[80:95]
	s_add_u32 m0, s46, 0x3000
	s_add_u32 s40, s40, 0x1800
	s_addc_u32 s41, s41, 0
	global_load_lds_dwordx4 v76, s[40:41]
	v_mfma_f32_32x32x16_f16 a[64:79], v[32:35], v[0:3], a[64:79]
	s_add_u32 m0, s47, 0x3000
	s_add_u32 s42, s42, 0x1800
	s_addc_u32 s43, s43, 0
	global_load_lds_dwordx4 v77, s[42:43]
	v_mfma_f32_32x32x16_f16 a[48:63], v[36:39], v[0:3], a[48:63]
	s_add_u32 m0, s48, 0x3000
	s_add_u32 s44, s44, 0x1800
	s_addc_u32 s45, s45, 0
	global_load_lds_dwordx4 v78, s[44:45]
	v_mfma_f32_32x32x16_f16 a[32:47], v[40:43], v[0:3], a[32:47]
	v_mfma_f32_32x32x16_f16 a[16:31], v[44:47], v[0:3], a[16:31]
	v_mfma_f32_32x32x16_f16 a[0:15], v[48:51], v[0:3], a[0:15]
	s_waitcnt lgkmcnt(6)
	ds_read_b128 v[28:31], v84 offset:60352
	ds_read_b128 v[32:35], v84 offset:61376
	ds_read_b128 v[36:39], v84 offset:62400
	ds_read_b128 v[40:43], v84 offset:63424
	ds_read_b128 v[44:47], v84 offset:64448
	ds_read_b128 v[48:51], v84 offset:65472
	s_waitcnt lgkmcnt(6)
	v_mfma_f32_32x32x16_f16 a[80:95], v[4:7], v[100:103], a[80:95]
	v_mfma_f32_32x32x16_f16 a[64:79], v[8:11], v[100:103], a[64:79]
	v_mfma_f32_32x32x16_f16 a[48:63], v[12:15], v[100:103], a[48:63]
	s_waitcnt vmcnt(10)
	s_waitcnt lgkmcnt(0)
	s_barrier
	ds_read_b128 v[4:7], v98
	ds_read_b128 v[8:11], v98 offset:1024
	ds_read_b128 v[12:15], v98 offset:2048
	v_mfma_f32_32x32x16_f16 a[32:47], v[16:19], v[100:103], a[32:47]
	ds_read_b128 v[16:19], v98 offset:3072
	v_mfma_f32_32x32x16_f16 a[16:31], v[20:23], v[100:103], a[16:31]
	ds_read_b128 v[20:23], v98 offset:4096
	v_mfma_f32_32x32x16_f16 a[0:15], v[24:27], v[100:103], a[0:15]
	ds_read_b128 v[24:27], v98 offset:5120
	v_mfma_f32_32x32x16_f16 a[80:95], v[28:31], v[104:107], a[80:95]
	s_add_u32 m0, s46, 0xd3c0
	s_add_u32 s40, s40, 0x1800
	s_addc_u32 s41, s41, 0
	global_load_lds_dwordx4 v76, s[40:41]
	v_mfma_f32_32x32x16_f16 a[64:79], v[32:35], v[104:107], a[64:79]
	s_add_u32 m0, s47, 0xd3c0
	s_add_u32 s42, s42, 0x1800
	s_addc_u32 s43, s43, 0
	global_load_lds_dwordx4 v77, s[42:43]
	v_mfma_f32_32x32x16_f16 a[48:63], v[36:39], v[104:107], a[48:63]
	s_add_u32 m0, s48, 0xd3c0
	s_add_u32 s44, s44, 0x1800
	s_addc_u32 s45, s45, 0
	global_load_lds_dwordx4 v78, s[44:45]
	v_mfma_f32_32x32x16_f16 a[32:47], v[40:43], v[104:107], a[32:47]
	v_mfma_f32_32x32x16_f16 a[16:31], v[44:47], v[104:107], a[16:31]
	v_mfma_f32_32x32x16_f16 a[0:15], v[48:51], v[104:107], a[0:15]
	ds_read_b128 v[28:31], v98 offset:6144
	ds_read_b128 v[32:35], v98 offset:7168
	ds_read_b128 v[36:39], v98 offset:8192
	ds_read_b128 v[40:43], v98 offset:9216
	ds_read_b128 v[44:47], v98 offset:10240
	ds_read_b128 v[48:51], v98 offset:11264
	s_waitcnt lgkmcnt(6)
	v_mfma_f32_32x32x16_f16 a[80:95], v[4:7], v[108:111], a[80:95]
	s_waitcnt vmcnt(26)
	ds_write_b128 v81, v[132:135]
	ds_write_b128 v81, v[136:139] offset:1024
	ds_write_b128 v81, v[140:143] offset:2048
	ds_write_b128 v81, v[144:147] offset:3072
	v_mfma_f32_32x32x16_f16 a[64:79], v[8:11], v[108:111], a[64:79]
	ds_read_b128 v[52:55], v95
	ds_read_b128 v[56:59], v96
	ds_read_b128 v[60:63], v97
	ds_read_b128 v[0:3], v94
	v_mfma_f32_32x32x16_f16 a[48:63], v[12:15], v[108:111], a[48:63]
	s_waitcnt vmcnt(10)
	s_waitcnt lgkmcnt(8)
	s_barrier
	ds_read_b128 v[4:7], v84 offset:0
	ds_read_b128 v[8:11], v84 offset:1024
	ds_read_b128 v[12:15], v84 offset:2048
	v_mfma_f32_32x32x16_f16 a[32:47], v[16:19], v[108:111], a[32:47]
	ds_read_b128 v[16:19], v84 offset:3072
	v_mfma_f32_32x32x16_f16 a[16:31], v[20:23], v[108:111], a[16:31]
	ds_read_b128 v[20:23], v84 offset:4096
	v_mfma_f32_32x32x16_f16 a[0:15], v[24:27], v[108:111], a[0:15]
	ds_read_b128 v[24:27], v84 offset:5120
	v_mfma_f32_32x32x16_f16 a[80:95], v[28:31], v[112:115], a[80:95]
	s_add_u32 m0, s46, 0x103c0
	s_add_u32 s40, s40, 0x1800
	s_addc_u32 s41, s41, 0
	global_load_lds_dwordx4 v76, s[40:41]
	v_mfma_f32_32x32x16_f16 a[64:79], v[32:35], v[112:115], a[64:79]
	s_add_u32 m0, s47, 0x103c0
	s_add_u32 s42, s42, 0x1800
	s_addc_u32 s43, s43, 0
	global_load_lds_dwordx4 v77, s[42:43]
	v_mfma_f32_32x32x16_f16 a[48:63], v[36:39], v[112:115], a[48:63]
	s_add_u32 m0, s48, 0x103c0
	s_add_u32 s44, s44, 0x1800
	s_addc_u32 s45, s45, 0
	global_load_lds_dwordx4 v78, s[44:45]
	v_mfma_f32_32x32x16_f16 a[32:47], v[40:43], v[112:115], a[32:47]
	v_mfma_f32_32x32x16_f16 a[16:31], v[44:47], v[112:115], a[16:31]
	v_mfma_f32_32x32x16_f16 a[0:15], v[48:51], v[112:115], a[0:15]
	s_waitcnt lgkmcnt(6)
	ds_read_b128 v[28:31], v84 offset:6144
	ds_read_b128 v[32:35], v84 offset:7168
	ds_read_b128 v[36:39], v84 offset:8192
	ds_read_b128 v[40:43], v84 offset:9216
	ds_read_b128 v[44:47], v84 offset:10240
	ds_read_b128 v[48:51], v84 offset:11264
	s_waitcnt lgkmcnt(6)
	v_mfma_f32_32x32x16_f16 a[80:95], v[4:7], v[52:55], a[80:95]
	v_mfma_f32_32x32x16_f16 a[64:79], v[8:11], v[52:55], a[64:79]
	v_mfma_f32_32x32x16_f16 a[48:63], v[12:15], v[52:55], a[48:63]
	s_waitcnt vmcnt(6)
	s_waitcnt lgkmcnt(0)
	s_barrier
	ds_read_b128 v[4:7], v84 offset:12288
	ds_read_b128 v[8:11], v84 offset:13312
	ds_read_b128 v[12:15], v84 offset:14336
	v_mfma_f32_32x32x16_f16 a[32:47], v[16:19], v[52:55], a[32:47]
	ds_read_b128 v[16:19], v84 offset:15360
	v_mfma_f32_32x32x16_f16 a[16:31], v[20:23], v[52:55], a[16:31]
	ds_read_b128 v[20:23], v84 offset:16384
	v_mfma_f32_32x32x16_f16 a[0:15], v[24:27], v[52:55], a[0:15]
	ds_read_b128 v[24:27], v84 offset:17408
	v_mfma_f32_32x32x16_f16 a[80:95], v[28:31], v[56:59], a[80:95]
	s_add_u32 m0, s46, 0x0
	s_add_u32 s40, s40, 0x1800
	s_addc_u32 s41, s41, 0
	global_load_lds_dwordx4 v76, s[40:41]
	v_mfma_f32_32x32x16_f16 a[64:79], v[32:35], v[56:59], a[64:79]
	s_add_u32 m0, s47, 0x0
	s_add_u32 s42, s42, s49
	s_addc_u32 s43, s43, 0
	global_load_lds_dwordx4 v77, s[42:43]
	v_mfma_f32_32x32x16_f16 a[48:63], v[36:39], v[56:59], a[48:63]
	s_add_u32 m0, s48, 0x0
	s_add_u32 s44, s44, 0xc00
	s_addc_u32 s45, s45, 0
	global_load_lds_dwordx4 v78, s[44:45]
	v_mfma_f32_32x32x16_f16 a[32:47], v[40:43], v[56:59], a[32:47]
	v_mfma_f32_32x32x16_f16 a[16:31], v[44:47], v[56:59], a[16:31]
	v_mfma_f32_32x32x16_f16 a[0:15], v[48:51], v[56:59], a[0:15]
	ds_read_b128 v[28:31], v84 offset:18432
	ds_read_b128 v[32:35], v84 offset:19456
	ds_read_b128 v[36:39], v84 offset:20480
	ds_read_b128 v[40:43], v84 offset:21504
	ds_read_b128 v[44:47], v84 offset:22528
	ds_read_b128 v[48:51], v84 offset:23552
	s_waitcnt lgkmcnt(6)
	v_mfma_f32_32x32x16_f16 a[80:95], v[4:7], v[60:63], a[80:95]
	s_waitcnt vmcnt(22)
	ds_write_b128 v81, v[148:151]
	ds_write_b128 v81, v[152:155] offset:1024
	ds_write_b128 v81, v[156:159] offset:2048
	ds_write_b128 v81, v[72:75] offset:3072
	v_mfma_f32_32x32x16_f16 a[64:79], v[8:11], v[60:63], a[64:79]
	ds_read_b128 v[100:103], v95
	ds_read_b128 v[104:107], v96
	ds_read_b128 v[108:111], v97
	ds_read_b128 v[112:115], v94
	v_mfma_f32_32x32x16_f16 a[48:63], v[12:15], v[60:63], a[48:63]
	s_waitcnt vmcnt(6)
	s_waitcnt lgkmcnt(8)
	s_barrier
	ds_read_b128 v[4:7], v84 offset:54208
	ds_read_b128 v[8:11], v84 offset:55232
	ds_read_b128 v[12:15], v84 offset:56256
	v_mfma_f32_32x32x16_f16 a[32:47], v[16:19], v[60:63], a[32:47]
	ds_read_b128 v[16:19], v84 offset:57280
	v_mfma_f32_32x32x16_f16 a[16:31], v[20:23], v[60:63], a[16:31]
	ds_read_b128 v[20:23], v84 offset:58304
	v_mfma_f32_32x32x16_f16 a[0:15], v[24:27], v[60:63], a[0:15]
	ds_read_b128 v[24:27], v84 offset:59328
	v_mfma_f32_32x32x16_f16 a[80:95], v[28:31], v[0:3], a[80:95]
	v_mfma_f32_32x32x16_f16 a[64:79], v[32:35], v[0:3], a[64:79]
	v_mfma_f32_32x32x16_f16 a[48:63], v[36:39], v[0:3], a[48:63]
	v_mfma_f32_32x32x16_f16 a[32:47], v[40:43], v[0:3], a[32:47]
	v_mfma_f32_32x32x16_f16 a[16:31], v[44:47], v[0:3], a[16:31]
	v_mfma_f32_32x32x16_f16 a[0:15], v[48:51], v[0:3], a[0:15]
	s_waitcnt lgkmcnt(6)
	ds_read_b128 v[28:31], v84 offset:60352
	ds_read_b128 v[32:35], v84 offset:61376
	ds_read_b128 v[36:39], v84 offset:62400
	ds_read_b128 v[40:43], v84 offset:63424
	ds_read_b128 v[44:47], v84 offset:64448
	ds_read_b128 v[48:51], v84 offset:65472
	s_waitcnt lgkmcnt(6)
	v_mfma_f32_32x32x16_f16 a[80:95], v[4:7], v[100:103], a[80:95]
	v_mfma_f32_32x32x16_f16 a[64:79], v[8:11], v[100:103], a[64:79]
	v_mfma_f32_32x32x16_f16 a[48:63], v[12:15], v[100:103], a[48:63]
	s_waitcnt vmcnt(3)
	s_waitcnt lgkmcnt(0)
	s_barrier
	ds_read_b128 v[4:7], v98
	ds_read_b128 v[8:11], v98 offset:1024
	ds_read_b128 v[12:15], v98 offset:2048
	v_mfma_f32_32x32x16_f16 a[32:47], v[16:19], v[100:103], a[32:47]
	ds_read_b128 v[16:19], v98 offset:3072
	v_mfma_f32_32x32x16_f16 a[16:31], v[20:23], v[100:103], a[16:31]
	ds_read_b128 v[20:23], v98 offset:4096
	v_mfma_f32_32x32x16_f16 a[0:15], v[24:27], v[100:103], a[0:15]
	ds_read_b128 v[24:27], v98 offset:5120
	v_mfma_f32_32x32x16_f16 a[80:95], v[28:31], v[104:107], a[80:95]
	v_mfma_f32_32x32x16_f16 a[64:79], v[32:35], v[104:107], a[64:79]
	v_mfma_f32_32x32x16_f16 a[48:63], v[36:39], v[104:107], a[48:63]
	v_mfma_f32_32x32x16_f16 a[32:47], v[40:43], v[104:107], a[32:47]
	v_mfma_f32_32x32x16_f16 a[16:31], v[44:47], v[104:107], a[16:31]
	v_mfma_f32_32x32x16_f16 a[0:15], v[48:51], v[104:107], a[0:15]
	ds_read_b128 v[28:31], v98 offset:6144
	ds_read_b128 v[32:35], v98 offset:7168
	ds_read_b128 v[36:39], v98 offset:8192
	ds_read_b128 v[40:43], v98 offset:9216
	ds_read_b128 v[44:47], v98 offset:10240
	ds_read_b128 v[48:51], v98 offset:11264
	s_waitcnt lgkmcnt(6)
	v_mfma_f32_32x32x16_f16 a[80:95], v[4:7], v[108:111], a[80:95]
	s_waitcnt vmcnt(12)
	ds_write_b128 v81, v[116:119]
	ds_write_b128 v81, v[120:123] offset:1024
	ds_write_b128 v81, v[124:127] offset:2048
	ds_write_b128 v81, v[128:131] offset:3072
	v_mfma_f32_32x32x16_f16 a[64:79], v[8:11], v[108:111], a[64:79]
	ds_read_b128 v[0:3], v94
	v_mfma_f32_32x32x16_f16 a[48:63], v[12:15], v[108:111], a[48:63]
	s_waitcnt vmcnt(0)
	s_waitcnt lgkmcnt(5)
	s_barrier
	ds_read_b128 v[4:7], v84 offset:0
	ds_read_b128 v[8:11], v84 offset:1024
	ds_read_b128 v[12:15], v84 offset:2048
	v_mfma_f32_32x32x16_f16 a[32:47], v[16:19], v[108:111], a[32:47]
	ds_read_b128 v[16:19], v84 offset:3072
	v_mfma_f32_32x32x16_f16 a[16:31], v[20:23], v[108:111], a[16:31]
	ds_read_b128 v[20:23], v84 offset:4096
	v_mfma_f32_32x32x16_f16 a[0:15], v[24:27], v[108:111], a[0:15]
	ds_read_b128 v[24:27], v84 offset:5120
	v_mfma_f32_32x32x16_f16 a[80:95], v[28:31], v[112:115], a[80:95]
	v_mfma_f32_32x32x16_f16 a[64:79], v[32:35], v[112:115], a[64:79]
	v_mfma_f32_32x32x16_f16 a[48:63], v[36:39], v[112:115], a[48:63]
	v_mfma_f32_32x32x16_f16 a[32:47], v[40:43], v[112:115], a[32:47]
	v_mfma_f32_32x32x16_f16 a[16:31], v[44:47], v[112:115], a[16:31]
	v_mfma_f32_32x32x16_f16 a[0:15], v[48:51], v[112:115], a[0:15]
	s_waitcnt lgkmcnt(0)
	v_mfma_f32_32x32x16_f16 a[80:95], v[4:7], v[0:3], a[80:95]
	v_mfma_f32_32x32x16_f16 a[16:31], v[20:23], v[0:3], a[16:31]
	v_lshlrev_b32_e32 v22, 4, v85
	v_mfma_f32_32x32x16_f16 a[64:79], v[8:11], v[0:3], a[64:79]
	v_mfma_f32_32x32x16_f16 a[48:63], v[12:15], v[0:3], a[48:63]
	s_nop 7
	v_accvgpr_read_b32 v13, a88
	v_mfma_f32_32x32x16_f16 a[32:47], v[16:19], v[0:3], a[32:47]
	v_accvgpr_read_b32 v17, a92
	v_mfma_f32_32x32x16_f16 a[0:15], v[24:27], v[0:3], a[0:15]
	ds_read_b128 v[2:5], v22 offset:53248
	ds_read_b128 v[6:9], v22 offset:53280
	v_accvgpr_read_b32 v1, a80
	v_lshlrev_b32_e32 v0, 4, v92
	s_waitcnt lgkmcnt(1)
	v_add_f32_e32 v1, v1, v2
	v_accvgpr_read_b32 v2, a81
	v_add_f32_e32 v2, v3, v2
	v_max_f32_e32 v10, 0, v2
	v_accvgpr_read_b32 v2, a82
	v_add_f32_e32 v2, v4, v2
	v_max_f32_e32 v11, 0, v2
	v_accvgpr_read_b32 v2, a83
	v_add_f32_e32 v2, v5, v2
	v_max_f32_e32 v12, 0, v2
	v_accvgpr_read_b32 v2, a84
	s_waitcnt lgkmcnt(0)
	v_add_f32_e32 v2, v2, v6
	v_max_f32_e32 v6, 0, v2
	v_accvgpr_read_b32 v2, a85
	v_add_f32_e32 v2, v7, v2
	v_max_f32_e32 v7, 0, v2
	v_accvgpr_read_b32 v2, a86
	v_add_f32_e32 v2, v8, v2
	v_max_f32_e32 v8, 0, v2
	v_accvgpr_read_b32 v2, a87
	v_add_f32_e32 v2, v9, v2
	v_max_f32_e32 v9, 0, v2
	ds_read_b128 v[2:5], v22 offset:53312
	v_max_f32_e32 v1, 0, v1
	s_waitcnt lgkmcnt(0)
	v_add_f32_e32 v2, v13, v2
	v_max_f32_e32 v13, 0, v2
	v_accvgpr_read_b32 v2, a89
	v_add_f32_e32 v2, v3, v2
	v_max_f32_e32 v14, 0, v2
	v_accvgpr_read_b32 v2, a90
	v_add_f32_e32 v2, v4, v2
	v_max_f32_e32 v15, 0, v2
	v_accvgpr_read_b32 v2, a91
	v_add_f32_e32 v2, v5, v2
	v_max_f32_e32 v16, 0, v2
	ds_read_b128 v[2:5], v22 offset:53344
	s_waitcnt lgkmcnt(0)
	v_add_f32_e32 v2, v17, v2
	v_max_f32_e32 v17, 0, v2
	v_accvgpr_read_b32 v2, a93
	v_add_f32_e32 v2, v3, v2
	v_max_f32_e32 v18, 0, v2
	v_accvgpr_read_b32 v2, a94
	v_add_f32_e32 v2, v4, v2
	v_max_f32_e32 v19, 0, v2
	v_accvgpr_read_b32 v2, a95
	v_add_f32_e32 v2, v5, v2
	v_cvt_pk_f16_f32 v5, v8, v9
	v_cvt_pk_f16_f32 v4, v6, v7
	ds_read_b128 v[6:9], v0 offset:40960
	v_max_f32_e32 v20, 0, v2
	v_cvt_pk_f16_f32 v3, v11, v12
	v_cvt_pk_f16_f32 v2, v1, v10
	v_accvgpr_read_b32 v1, a64
	s_waitcnt lgkmcnt(0)
	v_mfma_f32_32x32x16_f16 a[80:95], v[6:9], v[2:5], 0
	ds_read_b128 v[6:9], v0 offset:41984
	v_cvt_pk_f16_f32 v5, v19, v20
	v_cvt_pk_f16_f32 v4, v17, v18
	v_cvt_pk_f16_f32 v3, v15, v16
	v_cvt_pk_f16_f32 v2, v13, v14
	v_accvgpr_read_b32 v13, a72
	v_accvgpr_read_b32 v17, a76
	s_waitcnt lgkmcnt(0)
	v_mfma_f32_32x32x16_f16 a[80:95], v[6:9], v[2:5], a[80:95]
	ds_read_b128 v[2:5], v22 offset:53376
	v_accvgpr_read_b32 v9, a68
	s_waitcnt lgkmcnt(0)
	v_add_f32_e32 v1, v1, v2
	v_accvgpr_read_b32 v2, a65
	v_add_f32_e32 v2, v3, v2
	v_max_f32_e32 v6, 0, v2
	v_accvgpr_read_b32 v2, a66
	v_add_f32_e32 v2, v4, v2
	v_max_f32_e32 v7, 0, v2
	v_accvgpr_read_b32 v2, a67
	v_add_f32_e32 v2, v5, v2
	v_max_f32_e32 v8, 0, v2
	ds_read_b128 v[2:5], v22 offset:53408
	v_max_f32_e32 v1, 0, v1
	s_waitcnt lgkmcnt(0)
	v_add_f32_e32 v2, v9, v2
	v_max_f32_e32 v9, 0, v2
	v_accvgpr_read_b32 v2, a69
	v_add_f32_e32 v2, v3, v2
	v_max_f32_e32 v10, 0, v2
	v_accvgpr_read_b32 v2, a70
	v_add_f32_e32 v2, v4, v2
	v_max_f32_e32 v11, 0, v2
	v_accvgpr_read_b32 v2, a71
	v_add_f32_e32 v2, v5, v2
	v_max_f32_e32 v12, 0, v2
	ds_read_b128 v[2:5], v22 offset:53440
	s_waitcnt lgkmcnt(0)
	v_add_f32_e32 v2, v13, v2
	v_max_f32_e32 v13, 0, v2
	v_accvgpr_read_b32 v2, a73
	v_add_f32_e32 v2, v3, v2
	v_max_f32_e32 v14, 0, v2
	v_accvgpr_read_b32 v2, a74
	v_add_f32_e32 v2, v4, v2
	v_max_f32_e32 v15, 0, v2
	v_accvgpr_read_b32 v2, a75
	v_add_f32_e32 v2, v5, v2
	v_max_f32_e32 v16, 0, v2
	ds_read_b128 v[2:5], v22 offset:53472
	s_waitcnt lgkmcnt(0)
	v_add_f32_e32 v2, v17, v2
	v_max_f32_e32 v17, 0, v2
	v_accvgpr_read_b32 v2, a77
	v_add_f32_e32 v2, v3, v2
	v_max_f32_e32 v18, 0, v2
	v_accvgpr_read_b32 v2, a78
	v_add_f32_e32 v2, v4, v2
	v_max_f32_e32 v19, 0, v2
	v_accvgpr_read_b32 v2, a79
	v_add_f32_e32 v2, v5, v2
	v_max_f32_e32 v20, 0, v2
	v_cvt_pk_f16_f32 v4, v9, v10
	v_cvt_pk_f16_f32 v3, v7, v8
	v_cvt_pk_f16_f32 v2, v1, v6
	ds_read_b128 v[6:9], v0 offset:43008
	v_cvt_pk_f16_f32 v5, v11, v12
	v_accvgpr_read_b32 v1, a48
	s_waitcnt lgkmcnt(0)
	v_mfma_f32_32x32x16_f16 a[80:95], v[6:9], v[2:5], a[80:95]
	ds_read_b128 v[6:9], v0 offset:44032
	v_cvt_pk_f16_f32 v5, v19, v20
	v_cvt_pk_f16_f32 v4, v17, v18
	v_cvt_pk_f16_f32 v3, v15, v16
	v_cvt_pk_f16_f32 v2, v13, v14
	v_accvgpr_read_b32 v13, a56
	v_accvgpr_read_b32 v17, a60
	s_waitcnt lgkmcnt(0)
	v_mfma_f32_32x32x16_f16 a[80:95], v[6:9], v[2:5], a[80:95]
	ds_read_b128 v[2:5], v22 offset:53504
	v_accvgpr_read_b32 v9, a52
	s_waitcnt lgkmcnt(0)
	v_add_f32_e32 v1, v1, v2
	v_accvgpr_read_b32 v2, a49
	v_add_f32_e32 v2, v3, v2
	v_max_f32_e32 v6, 0, v2
	v_accvgpr_read_b32 v2, a50
	v_add_f32_e32 v2, v4, v2
	v_max_f32_e32 v7, 0, v2
	v_accvgpr_read_b32 v2, a51
	v_add_f32_e32 v2, v5, v2
	v_max_f32_e32 v8, 0, v2
	ds_read_b128 v[2:5], v22 offset:53536
	v_max_f32_e32 v1, 0, v1
	s_waitcnt lgkmcnt(0)
	v_add_f32_e32 v2, v9, v2
	v_max_f32_e32 v9, 0, v2
	v_accvgpr_read_b32 v2, a53
	v_add_f32_e32 v2, v3, v2
	v_max_f32_e32 v10, 0, v2
	v_accvgpr_read_b32 v2, a54
	v_add_f32_e32 v2, v4, v2
	v_max_f32_e32 v11, 0, v2
	v_accvgpr_read_b32 v2, a55
	v_add_f32_e32 v2, v5, v2
	v_max_f32_e32 v12, 0, v2
	ds_read_b128 v[2:5], v22 offset:53568
	s_waitcnt lgkmcnt(0)
	v_add_f32_e32 v2, v13, v2
	v_max_f32_e32 v13, 0, v2
	v_accvgpr_read_b32 v2, a57
	v_add_f32_e32 v2, v3, v2
	v_max_f32_e32 v14, 0, v2
	v_accvgpr_read_b32 v2, a58
	v_add_f32_e32 v2, v4, v2
	v_max_f32_e32 v15, 0, v2
	v_accvgpr_read_b32 v2, a59
	v_add_f32_e32 v2, v5, v2
	v_max_f32_e32 v16, 0, v2
	ds_read_b128 v[2:5], v22 offset:53600
	s_waitcnt lgkmcnt(0)
	v_add_f32_e32 v2, v17, v2
	v_max_f32_e32 v17, 0, v2
	v_accvgpr_read_b32 v2, a61
	v_add_f32_e32 v2, v3, v2
	v_max_f32_e32 v18, 0, v2
	v_accvgpr_read_b32 v2, a62
	v_add_f32_e32 v2, v4, v2
	v_max_f32_e32 v19, 0, v2
	v_accvgpr_read_b32 v2, a63
	v_add_f32_e32 v2, v5, v2
	v_max_f32_e32 v20, 0, v2
	v_cvt_pk_f16_f32 v4, v9, v10
	v_cvt_pk_f16_f32 v3, v7, v8
	v_cvt_pk_f16_f32 v2, v1, v6
	ds_read_b128 v[6:9], v0 offset:45056
	v_cvt_pk_f16_f32 v5, v11, v12
	v_accvgpr_read_b32 v1, a32
	s_waitcnt lgkmcnt(0)
	v_mfma_f32_32x32x16_f16 a[80:95], v[6:9], v[2:5], a[80:95]
	ds_read_b128 v[6:9], v0 offset:46080
	v_cvt_pk_f16_f32 v5, v19, v20
	v_cvt_pk_f16_f32 v4, v17, v18
	v_cvt_pk_f16_f32 v3, v15, v16
	v_cvt_pk_f16_f32 v2, v13, v14
	v_accvgpr_read_b32 v13, a40
	v_accvgpr_read_b32 v17, a44
	s_waitcnt lgkmcnt(0)
	v_mfma_f32_32x32x16_f16 a[80:95], v[6:9], v[2:5], a[80:95]
	ds_read_b128 v[2:5], v22 offset:53632
	v_accvgpr_read_b32 v9, a36
	s_waitcnt lgkmcnt(0)
	v_add_f32_e32 v1, v1, v2
	v_accvgpr_read_b32 v2, a33
	v_add_f32_e32 v2, v3, v2
	v_max_f32_e32 v6, 0, v2
	v_accvgpr_read_b32 v2, a34
	v_add_f32_e32 v2, v4, v2
	v_max_f32_e32 v7, 0, v2
	v_accvgpr_read_b32 v2, a35
	v_add_f32_e32 v2, v5, v2
	v_max_f32_e32 v8, 0, v2
	ds_read_b128 v[2:5], v22 offset:53664
	v_max_f32_e32 v1, 0, v1
	s_waitcnt lgkmcnt(0)
	v_add_f32_e32 v2, v9, v2
	v_max_f32_e32 v9, 0, v2
	v_accvgpr_read_b32 v2, a37
	v_add_f32_e32 v2, v3, v2
	v_max_f32_e32 v10, 0, v2
	v_accvgpr_read_b32 v2, a38
	v_add_f32_e32 v2, v4, v2
	v_max_f32_e32 v11, 0, v2
	v_accvgpr_read_b32 v2, a39
	v_add_f32_e32 v2, v5, v2
	v_max_f32_e32 v12, 0, v2
	ds_read_b128 v[2:5], v22 offset:53696
	s_waitcnt lgkmcnt(0)
	v_add_f32_e32 v2, v13, v2
	v_max_f32_e32 v13, 0, v2
	v_accvgpr_read_b32 v2, a41
	v_add_f32_e32 v2, v3, v2
	v_max_f32_e32 v14, 0, v2
	v_accvgpr_read_b32 v2, a42
	v_add_f32_e32 v2, v4, v2
	v_max_f32_e32 v15, 0, v2
	v_accvgpr_read_b32 v2, a43
	v_add_f32_e32 v2, v5, v2
	v_max_f32_e32 v16, 0, v2
	ds_read_b128 v[2:5], v22 offset:53728
	s_waitcnt lgkmcnt(0)
	v_add_f32_e32 v2, v17, v2
	v_max_f32_e32 v17, 0, v2
	v_accvgpr_read_b32 v2, a45
	v_add_f32_e32 v2, v3, v2
	v_max_f32_e32 v18, 0, v2
	v_accvgpr_read_b32 v2, a46
	v_add_f32_e32 v2, v4, v2
	v_max_f32_e32 v19, 0, v2
	v_accvgpr_read_b32 v2, a47
	v_add_f32_e32 v2, v5, v2
	v_max_f32_e32 v20, 0, v2
	v_cvt_pk_f16_f32 v4, v9, v10
	v_cvt_pk_f16_f32 v3, v7, v8
	v_cvt_pk_f16_f32 v2, v1, v6
	ds_read_b128 v[6:9], v0 offset:47104
	v_cvt_pk_f16_f32 v5, v11, v12
	v_accvgpr_read_b32 v1, a16
	s_waitcnt lgkmcnt(0)
	v_mfma_f32_32x32x16_f16 a[32:47], v[6:9], v[2:5], 0
	ds_read_b128 v[6:9], v0 offset:48128
	v_cvt_pk_f16_f32 v5, v19, v20
	v_cvt_pk_f16_f32 v4, v17, v18
	v_cvt_pk_f16_f32 v3, v15, v16
	v_cvt_pk_f16_f32 v2, v13, v14
	v_accvgpr_read_b32 v13, a24
	v_accvgpr_read_b32 v17, a28
	s_waitcnt lgkmcnt(0)
	v_mfma_f32_32x32x16_f16 a[32:47], v[6:9], v[2:5], a[32:47]
	ds_read_b128 v[2:5], v22 offset:53760
	v_accvgpr_read_b32 v9, a20
	s_waitcnt lgkmcnt(0)
	v_add_f32_e32 v1, v1, v2
	v_accvgpr_read_b32 v2, a17
	v_add_f32_e32 v2, v3, v2
	v_max_f32_e32 v6, 0, v2
	v_accvgpr_read_b32 v2, a18
	v_add_f32_e32 v2, v4, v2
	v_max_f32_e32 v7, 0, v2
	v_accvgpr_read_b32 v2, a19
	v_add_f32_e32 v2, v5, v2
	v_max_f32_e32 v8, 0, v2
	ds_read_b128 v[2:5], v22 offset:53792
	v_max_f32_e32 v1, 0, v1
	s_waitcnt lgkmcnt(0)
	v_add_f32_e32 v2, v9, v2
	v_max_f32_e32 v9, 0, v2
	v_accvgpr_read_b32 v2, a21
	v_add_f32_e32 v2, v3, v2
	v_max_f32_e32 v10, 0, v2
	v_accvgpr_read_b32 v2, a22
	v_add_f32_e32 v2, v4, v2
	v_max_f32_e32 v11, 0, v2
	v_accvgpr_read_b32 v2, a23
	v_add_f32_e32 v2, v5, v2
	v_max_f32_e32 v12, 0, v2
	ds_read_b128 v[2:5], v22 offset:53824
	s_waitcnt lgkmcnt(0)
	v_add_f32_e32 v2, v13, v2
	v_max_f32_e32 v13, 0, v2
	v_accvgpr_read_b32 v2, a25
	v_add_f32_e32 v2, v3, v2
	v_max_f32_e32 v14, 0, v2
	v_accvgpr_read_b32 v2, a26
	v_add_f32_e32 v2, v4, v2
	v_max_f32_e32 v15, 0, v2
	v_accvgpr_read_b32 v2, a27
	v_add_f32_e32 v2, v5, v2
	v_max_f32_e32 v16, 0, v2
	ds_read_b128 v[2:5], v22 offset:53856
	s_waitcnt lgkmcnt(0)
	v_add_f32_e32 v2, v17, v2
	v_max_f32_e32 v17, 0, v2
	v_accvgpr_read_b32 v2, a29
	v_add_f32_e32 v2, v3, v2
	v_max_f32_e32 v18, 0, v2
	v_accvgpr_read_b32 v2, a30
	v_add_f32_e32 v2, v4, v2
	v_max_f32_e32 v19, 0, v2
	v_accvgpr_read_b32 v2, a31
	v_add_f32_e32 v2, v5, v2
	v_max_f32_e32 v20, 0, v2
	v_cvt_pk_f16_f32 v4, v9, v10
	v_cvt_pk_f16_f32 v3, v7, v8
	v_cvt_pk_f16_f32 v2, v1, v6
	ds_read_b128 v[6:9], v0 offset:49152
	v_cvt_pk_f16_f32 v5, v11, v12
	v_accvgpr_read_b32 v1, a0
	s_waitcnt lgkmcnt(0)
	v_mfma_f32_32x32x16_f16 a[32:47], v[6:9], v[2:5], a[32:47]
	ds_read_b128 v[6:9], v0 offset:50176
	v_cvt_pk_f16_f32 v5, v19, v20
	v_cvt_pk_f16_f32 v4, v17, v18
	v_cvt_pk_f16_f32 v3, v15, v16
	v_cvt_pk_f16_f32 v2, v13, v14
	v_accvgpr_read_b32 v13, a8
	v_accvgpr_read_b32 v17, a12
	s_waitcnt lgkmcnt(0)
	v_mfma_f32_32x32x16_f16 a[32:47], v[6:9], v[2:5], a[32:47]
	ds_read_b128 v[2:5], v22 offset:53888
	v_accvgpr_read_b32 v9, a4
	s_waitcnt lgkmcnt(0)
	v_add_f32_e32 v1, v1, v2
	v_accvgpr_read_b32 v2, a1
	v_add_f32_e32 v2, v3, v2
	v_max_f32_e32 v6, 0, v2
	v_accvgpr_read_b32 v2, a2
	v_add_f32_e32 v2, v4, v2
	v_max_f32_e32 v7, 0, v2
	v_accvgpr_read_b32 v2, a3
	v_add_f32_e32 v2, v5, v2
	v_max_f32_e32 v8, 0, v2
	ds_read_b128 v[2:5], v22 offset:53920
	v_max_f32_e32 v1, 0, v1
	s_waitcnt lgkmcnt(0)
	v_add_f32_e32 v2, v9, v2
	v_max_f32_e32 v9, 0, v2
	v_accvgpr_read_b32 v2, a5
	v_add_f32_e32 v2, v3, v2
	v_max_f32_e32 v10, 0, v2
	v_accvgpr_read_b32 v2, a6
	v_add_f32_e32 v2, v4, v2
	v_max_f32_e32 v11, 0, v2
	v_accvgpr_read_b32 v2, a7
	v_add_f32_e32 v2, v5, v2
	v_max_f32_e32 v12, 0, v2
	ds_read_b128 v[2:5], v22 offset:53952
	s_waitcnt lgkmcnt(0)
	v_add_f32_e32 v2, v13, v2
	v_max_f32_e32 v13, 0, v2
	v_accvgpr_read_b32 v2, a9
	v_add_f32_e32 v2, v3, v2
	v_max_f32_e32 v14, 0, v2
	v_accvgpr_read_b32 v2, a10
	v_add_f32_e32 v2, v4, v2
	v_max_f32_e32 v15, 0, v2
	v_accvgpr_read_b32 v2, a11
	v_add_f32_e32 v2, v5, v2
	v_max_f32_e32 v16, 0, v2
	ds_read_b128 v[2:5], v22 offset:53984
	s_waitcnt lgkmcnt(0)
	v_add_f32_e32 v2, v17, v2
	v_max_f32_e32 v17, 0, v2
	v_accvgpr_read_b32 v2, a13
	v_add_f32_e32 v2, v3, v2
	v_max_f32_e32 v18, 0, v2
	v_accvgpr_read_b32 v2, a14
	v_add_f32_e32 v2, v4, v2
	v_max_f32_e32 v19, 0, v2
	v_accvgpr_read_b32 v2, a15
	v_add_f32_e32 v2, v5, v2
	v_max_f32_e32 v20, 0, v2
	v_cvt_pk_f16_f32 v4, v9, v10
	v_cvt_pk_f16_f32 v3, v7, v8
	v_cvt_pk_f16_f32 v2, v1, v6
	ds_read_b128 v[6:9], v0 offset:51200
	v_cvt_pk_f16_f32 v5, v11, v12
	s_waitcnt lgkmcnt(0)
	s_nop 0
	v_mfma_f32_32x32x16_f16 a[32:47], v[6:9], v[2:5], a[32:47]
	ds_read_b128 v[6:9], v0 offset:52224
	v_cvt_pk_f16_f32 v5, v19, v20
	v_cvt_pk_f16_f32 v4, v17, v18
	v_cvt_pk_f16_f32 v3, v15, v16
	v_cvt_pk_f16_f32 v2, v13, v14
	s_waitcnt lgkmcnt(0)
	s_nop 0
	v_mfma_f32_32x32x16_f16 a[32:47], v[6:9], v[2:5], a[32:47]
	s_and_saveexec_b64 s[2:3], s[0:1]
	s_cbranch_execz .LBB3_39
	v_accvgpr_read_b32 v0, a80
	v_accvgpr_read_b32 v6, a86
	v_accvgpr_read_b32 v7, a87
	v_accvgpr_read_b32 v8, a88
	v_accvgpr_read_b32 v9, a89
	v_accvgpr_read_b32 v10, a90
	v_accvgpr_read_b32 v11, a91
	v_accvgpr_read_b32 v12, a92
	v_accvgpr_read_b32 v13, a93
	v_accvgpr_read_b32 v14, a94
	v_accvgpr_read_b32 v15, a95
	v_accvgpr_read_b32 v6, a32
	v_accvgpr_read_b32 v14, a40
	v_accvgpr_read_b32 v15, a41
	v_accvgpr_read_b32 v16, a42
	v_accvgpr_read_b32 v17, a43
	v_accvgpr_read_b32 v18, a44
	v_accvgpr_read_b32 v19, a45
	v_accvgpr_read_b32 v20, a46
	v_accvgpr_read_b32 v21, a47
	ds_read_b128 v[14:17], v22 offset:54016
	ds_read_b128 v[18:21], v22 offset:54080
	v_accvgpr_read_b32 v12, a38
	v_accvgpr_read_b32 v13, a39
	v_lshlrev_b32_e32 v24, 2, v85
	v_accvgpr_read_b32 v1, a81
	v_accvgpr_read_b32 v7, a33
	v_mad_i64_i32 v[12:13], s[0:1], v80, 40, s[18:19]
	v_ashrrev_i32_e32 v25, 31, v24
	v_accvgpr_read_b32 v3, a83
	v_accvgpr_read_b32 v9, a35
	v_lshl_add_u64 v[22:23], v[24:25], 2, v[12:13]
	v_mov_b32_e32 v25, v1
	s_waitcnt lgkmcnt(1)
	v_mov_b32_e32 v27, v15
	v_mov_b32_e32 v1, v7
	s_waitcnt lgkmcnt(0)
	v_mov_b32_e32 v15, v19
	v_accvgpr_read_b32 v2, a82
	v_accvgpr_read_b32 v8, a34
	v_pk_add_f32 v[0:1], v[0:1], v[14:15]
	v_mov_b32_e32 v7, v3
	v_mov_b32_e32 v15, v17
	v_mov_b32_e32 v3, v9
	v_mov_b32_e32 v17, v21
	v_mov_b32_e32 v24, v6
	v_mov_b32_e32 v26, v18
	v_mov_b32_e32 v6, v8
	v_mov_b32_e32 v14, v20
	v_pk_add_f32 v[2:3], v[2:3], v[16:17]
	v_pk_add_f32 v[24:25], v[24:25], v[26:27]
	s_waitcnt vmcnt(0)
	v_pk_mul_f32 v[0:1], v[82:83], v[0:1]
	v_pk_add_f32 v[6:7], v[6:7], v[14:15]
	v_pk_mul_f32 v[2:3], v[82:83], v[2:3]
	v_accvgpr_read_b32 v4, a84
	v_accvgpr_read_b32 v5, a85
	v_accvgpr_read_b32 v10, a36
	v_accvgpr_read_b32 v11, a37
	v_pk_fma_f32 v[0:1], v[82:83], v[24:25], v[0:1] op_sel:[1,0,0] op_sel_hi:[0,1,1]
	v_pk_fma_f32 v[2:3], v[82:83], v[6:7], v[2:3] op_sel:[1,0,0] op_sel_hi:[0,1,1]
	v_cmp_eq_u32_e32 vcc, 0, v85
	global_store_dwordx4 v[22:23], v[0:3], off
	s_and_b64 exec, exec, vcc
	s_cbranch_execz .LBB3_39
	s_mov_b32 s0, 0xd000
	v_add_u32_e64 v0, s0, 0
	ds_read2_b64 v[0:3], v0 offset0:100 offset1:108
	v_mov_b32_e32 v9, v5
	v_mov_b32_e32 v5, v11
	v_mov_b32_e32 v8, v10
	v_pk_mov_b32 v[6:7], v[82:83], v[82:83] op_sel:[1,0]
	s_waitcnt lgkmcnt(0)
	v_mov_b32_e32 v15, v1
	v_mov_b32_e32 v1, v3
	v_mov_b32_e32 v14, v2
	v_pk_add_f32 v[0:1], v[4:5], v[0:1]
	v_pk_add_f32 v[8:9], v[8:9], v[14:15]
	v_pk_mul_f32 v[0:1], v[82:83], v[0:1]
	s_nop 0
	v_pk_fma_f32 v[0:1], v[6:7], v[8:9], v[0:1]
	global_store_dwordx2 v[12:13], v[0:1], off offset:32

amdhsa.kernels:
  - .agpr_count:     0
    .args:
      - .actual_access:  read_only
        .address_space:  global
        .offset:         0
        .size:           8
        .value_kind:     global_buffer
      - .actual_access:  read_only
        .address_space:  global
        .offset:         8
        .size:           8
        .value_kind:     global_buffer
      - .actual_access:  read_only
        .address_space:  global
        .offset:         16
        .size:           8
        .value_kind:     global_buffer
      - .actual_access:  read_only
        .address_space:  global
        .offset:         24
        .size:           8
        .value_kind:     global_buffer
      - .actual_access:  write_only
        .address_space:  global
        .offset:         32
        .size:           8
        .value_kind:     global_buffer
    .group_segment_fixed_size: 0
    .kernarg_segment_align: 8
    .kernarg_segment_size: 40
    .language:       OpenCL C
    .language_version:
      - 2
      - 0
    .max_flat_workgroup_size: 256
    .name:           _Z11prep_kernelPKfS0_S0_S0_Pc
    .private_segment_fixed_size: 0
    .sgpr_count:     30
    .sgpr_spill_count: 0
    .symbol:         _Z11prep_kernelPKfS0_S0_S0_Pc.kd
    .uniform_work_group_size: 1
    .uses_dynamic_stack: false
    .vgpr_count:     20
    .vgpr_spill_count: 0
    .wavefront_size: 64
  - .agpr_count:     0
    .args:
      - .address_space:  global
        .offset:         0
        .size:           8
        .value_kind:     global_buffer
      - .actual_access:  read_only
        .address_space:  global
        .offset:         8
        .size:           8
        .value_kind:     global_buffer
      - .actual_access:  read_only
        .address_space:  global
        .offset:         16
        .size:           8
        .value_kind:     global_buffer
      - .address_space:  global
        .offset:         24
        .size:           8
        .value_kind:     global_buffer
      - .actual_access:  write_only
        .address_space:  global
        .offset:         32
        .size:           8
        .value_kind:     global_buffer
      - .address_space:  global
        .offset:         40
        .size:           8
        .value_kind:     global_buffer
    .group_segment_fixed_size: 133120
    .kernarg_segment_align: 8
    .kernarg_segment_size: 48
    .language:       OpenCL C
    .language_version:
      - 2
      - 0
    .max_flat_workgroup_size: 512
    .name:           _Z13router_kernelPKfS0_S0_PcPfS1_
    .private_segment_fixed_size: 0
    .sgpr_count:     106
    .sgpr_spill_count: 7
    .symbol:         _Z13router_kernelPKfS0_S0_PcPfS1_.kd
    .uniform_work_group_size: 1
    .uses_dynamic_stack: false
    .vgpr_count:     239
    .vgpr_spill_count: 0
    .wavefront_size: 64
  - .agpr_count:     0
    .args:
      - .address_space:  global
        .offset:         0
        .size:           8
        .value_kind:     global_buffer
    .group_segment_fixed_size: 20
    .kernarg_segment_align: 8
    .kernarg_segment_size: 8
    .language:       OpenCL C
    .language_version:
      - 2
      - 0
    .max_flat_workgroup_size: 320
    .name:           _Z11plan_kernelPc
    .private_segment_fixed_size: 0
    .sgpr_count:     16
    .sgpr_spill_count: 0
    .symbol:         _Z11plan_kernelPc.kd
    .uniform_work_group_size: 1
    .uses_dynamic_stack: false
    .vgpr_count:     20
    .vgpr_spill_count: 0
    .wavefront_size: 64
  - .agpr_count:     96
    .args:
      - .actual_access:  read_only
        .address_space:  global
        .offset:         0
        .size:           8
        .value_kind:     global_buffer
      - .actual_access:  read_only
        .address_space:  global
        .offset:         8
        .size:           8
        .value_kind:     global_buffer
      - .address_space:  global
        .offset:         16
        .size:           8
        .value_kind:     global_buffer
      - .actual_access:  write_only
        .address_space:  global
        .offset:         24
        .size:           8
        .value_kind:     global_buffer
    .group_segment_fixed_size: 78784
    .kernarg_segment_align: 8
    .kernarg_segment_size: 32
    .language:       OpenCL C
    .language_version:
      - 2
      - 0
    .max_flat_workgroup_size: 256
    .name:           _Z13expert_kernelPKfS0_PKcPf
    .private_segment_fixed_size: 0
    .sgpr_count:     68
    .sgpr_spill_count: 0
    .symbol:         _Z13expert_kernelPKfS0_PKcPf.kd
    .uniform_work_group_size: 1
    .uses_dynamic_stack: false
    .vgpr_count:     256
    .vgpr_spill_count: 0
    .wavefront_size: 64
